# plus hoisted thread-invariant gather-index arithmetic in the up GEMM and the same first-K-tile peel for the three bf16 GEMM loops
# speedup vs baseline: 1.0119x; 1.0052x over previous
.LBB0_169:
	v_bfe_u32 v131, v0, 4, 2
	v_and_b32_e32 v130, 15, v0
	v_lshlrev_b32_e32 v2, 4, v131
	v_lshlrev_b32_e32 v4, 2, v0
	v_lshl_or_b32 v3, v130, 6, v2
	s_lshl_b32 s3, s13, 13
	v_and_b32_e32 v4, 32, v4
	v_bitop3_b32 v3, v3, s3, v4 bitop3:0xde
	s_lshl_b32 s3, s16, 5
	s_lshl_b32 s2, s13, 6
	s_and_b32 s3, s3, 0x60
	v_lshlrev_b32_e32 v5, 6, v0
	s_movk_i32 s13, 0x3c0
	v_and_or_b32 v2, v5, s13, v2
	s_lshl_b32 s13, s3, 7
	s_add_u32 s16, s8, 0x80
	v_bitop3_b32 v4, s13, v2, v4 bitop3:0xf6
	s_waitcnt vmcnt(2)
	s_barrier
	s_addc_u32 s17, s9, 0
	s_add_i32 s34, s5, 0x18000
	s_mov_b32 s13, m0
	s_mov_b32 m0, s34
	s_nop 2
	global_load_lds_dwordx4 v133, s[16:17]
	s_mov_b32 m0, s13
	s_add_i32 s35, s5, 0x1a000
	s_mov_b32 s13, m0
	s_mov_b32 m0, s35
	s_nop 2
	global_load_lds_dwordx4 v135, s[16:17]
	s_mov_b32 m0, s13
	s_add_u32 s16, s10, 0x80
	s_addc_u32 s17, s11, 0
	s_add_i32 s36, s5, 0x8000
	s_mov_b32 s13, m0
	s_mov_b32 m0, s36
	s_nop 2
	global_load_lds_dwordx4 v132, s[16:17]
	s_mov_b32 m0, s13
	s_add_i32 s37, s5, 0xa000
	s_mov_b32 s13, m0
	s_mov_b32 m0, s37
	s_nop 2
	global_load_lds_dwordx4 v134, s[16:17]
	s_mov_b32 m0, s13
	s_add_u32 s16, s8, 0x40080
	s_addc_u32 s17, s9, 0
	s_add_i32 s40, s5, 0x1c000
	s_mov_b32 s13, m0
	s_mov_b32 m0, s40
	s_nop 2
	global_load_lds_dwordx4 v133, s[16:17]
	s_mov_b32 m0, s13
	s_add_i32 s41, s5, 0x1e000
	s_mov_b32 s13, m0
	s_mov_b32 m0, s41
	s_nop 2
	global_load_lds_dwordx4 v135, s[16:17]
	s_mov_b32 m0, s13
	s_and_b32 s13, s93, 7
	s_lshl_b32 s13, s13, 22
	s_lshl_b32 s12, s12, 19
	s_add_i32 s52, s5, 0xc000
	s_add_i32 s53, s5, 0xe000
	s_or_b32 s12, s13, s12
	s_add_u32 s12, s74, s12
	s_addc_u32 s13, s75, 0
	s_add_u32 s12, s12, 0xd000000
	s_addc_u32 s13, s13, 0
	s_add_u32 s14, s74, s14
	s_waitcnt vmcnt(6)
	s_addc_u32 s15, s75, s15
	s_add_u32 s54, s14, 0x200100
	v_add_u32_e32 v4, 0, v4
	s_addc_u32 s55, s15, 0
	s_mov_b32 s56, -2
	v_add_u32_e32 v136, 0x10000, v4
	v_add_u32_e32 v137, 0x14000, v4
	v_add_u32_e32 v138, 0, v3
	v_add_u32_e32 v139, 0x18000, v4
	v_add_u32_e32 v140, 0x1c000, v4
	s_barrier
.Lpeel170:
	ds_read_b128 v[142:145], v136
	ds_read_b128 v[146:149], v136 offset:1024
	ds_read_b128 v[150:153], v136 offset:2048
	ds_read_b128 v[154:157], v136 offset:3072
	ds_read_b128 v[158:161], v137
	ds_read_b128 v[162:165], v137 offset:1024
	ds_read_b128 v[166:169], v137 offset:2048
	ds_read_b128 v[174:177], v137 offset:3072
	s_add_u32 s14, s12, 0x100
	s_addc_u32 s15, s13, 0
	s_cmp_eq_u32 s56, 12
	s_cselect_b32 s20, s10, s14
	s_cselect_b32 s21, s11, s15
	s_cselect_b32 s18, s8, s54
	s_cselect_b32 s19, s9, s55
	s_add_u32 s16, s20, 0x80
	s_addc_u32 s17, s21, 0
	ds_read_b128 v[178:181], v138
	ds_read_b128 v[182:185], v138 offset:1024
	ds_read_b128 v[186:189], v138 offset:2048
	ds_read_b128 v[190:193], v138 offset:3072
	ds_read_b128 v[194:197], v138 offset:4096
	ds_read_b128 v[198:201], v138 offset:5120
	ds_read_b128 v[202:205], v138 offset:6144
	ds_read_b128 v[206:209], v138 offset:7168
	s_add_u32 s12, s12, 0x40080
	s_addc_u32 s13, s13, 0
	s_mov_b32 s57, m0
	s_mov_b32 m0, s52
	s_nop 2
	global_load_lds_dwordx4 v132, s[12:13]
	s_mov_b32 m0, s57
	s_nop 0
	s_mov_b32 s57, m0
	s_mov_b32 m0, s53
	s_nop 2
	global_load_lds_dwordx4 v134, s[12:13]
	s_mov_b32 m0, s57
	s_waitcnt vmcnt(8)
	s_waitcnt lgkmcnt(0)
	s_barrier
	s_setprio 1
	s_waitcnt lgkmcnt(7)
	v_mfma_f32_16x16x32_bf16 v[126:129], v[142:145], v[178:181], 0
	v_mfma_f32_16x16x32_bf16 v[122:125], v[150:153], v[178:181], 0
	s_waitcnt lgkmcnt(5)
	v_mfma_f32_16x16x32_bf16 v[110:113], v[142:145], v[186:189], 0
	v_mfma_f32_16x16x32_bf16 v[106:109], v[150:153], v[186:189], 0
	s_waitcnt lgkmcnt(3)
	v_mfma_f32_16x16x32_bf16 v[94:97], v[142:145], v[194:197], 0
	v_mfma_f32_16x16x32_bf16 v[90:93], v[150:153], v[194:197], 0
	s_waitcnt lgkmcnt(1)
	v_mfma_f32_16x16x32_bf16 v[78:81], v[142:145], v[202:205], 0
	v_mfma_f32_16x16x32_bf16 v[74:77], v[150:153], v[202:205], 0
	v_mfma_f32_16x16x32_bf16 v[126:129], v[146:149], v[182:185], v[126:129]
	v_mfma_f32_16x16x32_bf16 v[122:125], v[154:157], v[182:185], v[122:125]
	v_mfma_f32_16x16x32_bf16 v[110:113], v[146:149], v[190:193], v[110:113]
	v_mfma_f32_16x16x32_bf16 v[106:109], v[154:157], v[190:193], v[106:109]
	v_mfma_f32_16x16x32_bf16 v[94:97], v[146:149], v[198:201], v[94:97]
	v_mfma_f32_16x16x32_bf16 v[90:93], v[154:157], v[198:201], v[90:93]
	s_waitcnt lgkmcnt(0)
	v_mfma_f32_16x16x32_bf16 v[78:81], v[146:149], v[206:209], v[78:81]
	v_mfma_f32_16x16x32_bf16 v[74:77], v[154:157], v[206:209], v[74:77]
	s_setprio 0
	s_setprio 1
	v_mfma_f32_16x16x32_bf16 v[118:121], v[158:161], v[178:181], 0
	v_mfma_f32_16x16x32_bf16 v[114:117], v[166:169], v[178:181], 0
	v_mfma_f32_16x16x32_bf16 v[102:105], v[158:161], v[186:189], 0
	v_mfma_f32_16x16x32_bf16 v[98:101], v[166:169], v[186:189], 0
	v_mfma_f32_16x16x32_bf16 v[86:89], v[158:161], v[194:197], 0
	v_mfma_f32_16x16x32_bf16 v[82:85], v[166:169], v[194:197], 0
	v_mfma_f32_16x16x32_bf16 v[70:73], v[158:161], v[202:205], 0
	v_mfma_f32_16x16x32_bf16 v[66:69], v[166:169], v[202:205], 0
	v_mfma_f32_16x16x32_bf16 v[118:121], v[162:165], v[182:185], v[118:121]
	v_mfma_f32_16x16x32_bf16 v[114:117], v[174:177], v[182:185], v[114:117]
	v_mfma_f32_16x16x32_bf16 v[102:105], v[162:165], v[190:193], v[102:105]
	v_mfma_f32_16x16x32_bf16 v[98:101], v[174:177], v[190:193], v[98:101]
	v_mfma_f32_16x16x32_bf16 v[86:89], v[162:165], v[198:201], v[86:89]
	v_mfma_f32_16x16x32_bf16 v[82:85], v[174:177], v[198:201], v[82:85]
	v_mfma_f32_16x16x32_bf16 v[70:73], v[162:165], v[206:209], v[70:73]
	v_mfma_f32_16x16x32_bf16 v[66:69], v[174:177], v[206:209], v[66:69]
	s_setprio 0
	s_barrier
	ds_read_b128 v[178:181], v138 offset:16384
	ds_read_b128 v[182:185], v138 offset:17408
	ds_read_b128 v[186:189], v138 offset:18432
	ds_read_b128 v[190:193], v138 offset:19456
	ds_read_b128 v[194:197], v138 offset:20480
	ds_read_b128 v[198:201], v138 offset:21504
	ds_read_b128 v[202:205], v138 offset:22528
	ds_read_b128 v[206:209], v138 offset:23552
	s_mov_b32 s12, m0
	s_mov_b32 m0, s24
	s_nop 2
	global_load_lds_dwordx4 v133, s[18:19]
	s_mov_b32 m0, s12
	s_nop 0
	s_mov_b32 s12, m0
	s_mov_b32 m0, s25
	s_nop 2
	global_load_lds_dwordx4 v135, s[18:19]
	s_mov_b32 m0, s12
	s_add_u32 s12, s18, 0x40000
	s_addc_u32 s13, s19, 0
	s_mov_b32 s57, m0
	s_mov_b32 m0, s28
	s_nop 2
	global_load_lds_dwordx4 v133, s[12:13]
	s_mov_b32 m0, s57
	s_nop 0
	s_mov_b32 s57, m0
	s_mov_b32 m0, s29
	s_nop 2
	global_load_lds_dwordx4 v135, s[12:13]
	s_mov_b32 m0, s57
	s_mov_b32 s12, m0
	s_mov_b32 m0, s5
	s_nop 2
	global_load_lds_dwordx4 v132, s[20:21]
	s_mov_b32 m0, s12
	s_nop 0
	s_mov_b32 s12, m0
	s_mov_b32 m0, s30
	s_nop 2
	global_load_lds_dwordx4 v134, s[20:21]
	s_mov_b32 m0, s12
	s_waitcnt vmcnt(8)
	s_waitcnt lgkmcnt(0)
	s_barrier
	s_setprio 1
	s_waitcnt lgkmcnt(7)
	v_mfma_f32_16x16x32_bf16 v[62:65], v[142:145], v[178:181], 0
	v_mfma_f32_16x16x32_bf16 v[58:61], v[150:153], v[178:181], 0
	s_waitcnt lgkmcnt(5)
	v_mfma_f32_16x16x32_bf16 v[46:49], v[142:145], v[186:189], 0
	v_mfma_f32_16x16x32_bf16 v[42:45], v[150:153], v[186:189], 0
	s_waitcnt lgkmcnt(3)
	v_mfma_f32_16x16x32_bf16 v[30:33], v[142:145], v[194:197], 0
	v_mfma_f32_16x16x32_bf16 v[26:29], v[150:153], v[194:197], 0
	s_waitcnt lgkmcnt(1)
	v_mfma_f32_16x16x32_bf16 v[14:17], v[142:145], v[202:205], 0
	v_mfma_f32_16x16x32_bf16 v[10:13], v[150:153], v[202:205], 0
	v_mfma_f32_16x16x32_bf16 v[62:65], v[146:149], v[182:185], v[62:65]
	v_mfma_f32_16x16x32_bf16 v[58:61], v[154:157], v[182:185], v[58:61]
	v_mfma_f32_16x16x32_bf16 v[46:49], v[146:149], v[190:193], v[46:49]
	v_mfma_f32_16x16x32_bf16 v[42:45], v[154:157], v[190:193], v[42:45]
	v_mfma_f32_16x16x32_bf16 v[30:33], v[146:149], v[198:201], v[30:33]
	v_mfma_f32_16x16x32_bf16 v[26:29], v[154:157], v[198:201], v[26:29]
	s_waitcnt lgkmcnt(0)
	v_mfma_f32_16x16x32_bf16 v[14:17], v[146:149], v[206:209], v[14:17]
	v_mfma_f32_16x16x32_bf16 v[10:13], v[154:157], v[206:209], v[10:13]
	s_setprio 0
	s_setprio 1
	v_mfma_f32_16x16x32_bf16 v[54:57], v[158:161], v[178:181], 0
	v_mfma_f32_16x16x32_bf16 v[50:53], v[166:169], v[178:181], 0
	v_mfma_f32_16x16x32_bf16 v[38:41], v[158:161], v[186:189], 0
	v_mfma_f32_16x16x32_bf16 v[34:37], v[166:169], v[186:189], 0
	v_mfma_f32_16x16x32_bf16 v[22:25], v[158:161], v[194:197], 0
	v_mfma_f32_16x16x32_bf16 v[18:21], v[166:169], v[194:197], 0
	v_mfma_f32_16x16x32_bf16 v[6:9], v[158:161], v[202:205], 0
	v_mfma_f32_16x16x32_bf16 v[2:5], v[166:169], v[202:205], 0
	v_mfma_f32_16x16x32_bf16 v[54:57], v[162:165], v[182:185], v[54:57]
	v_mfma_f32_16x16x32_bf16 v[50:53], v[174:177], v[182:185], v[50:53]
	v_mfma_f32_16x16x32_bf16 v[38:41], v[162:165], v[190:193], v[38:41]
	v_mfma_f32_16x16x32_bf16 v[34:37], v[174:177], v[190:193], v[34:37]
	v_mfma_f32_16x16x32_bf16 v[22:25], v[162:165], v[198:201], v[22:25]
	v_mfma_f32_16x16x32_bf16 v[18:21], v[174:177], v[198:201], v[18:21]
	v_mfma_f32_16x16x32_bf16 v[6:9], v[162:165], v[206:209], v[6:9]
	v_mfma_f32_16x16x32_bf16 v[2:5], v[174:177], v[206:209], v[2:5]
	s_setprio 0
	s_barrier
	s_branch .Lmid170

.Lmid170:
	ds_read_b128 v[142:145], v139
	ds_read_b128 v[146:149], v139 offset:1024
	ds_read_b128 v[150:153], v139 offset:2048
	ds_read_b128 v[154:157], v139 offset:3072
	ds_read_b128 v[158:161], v140
	ds_read_b128 v[162:165], v140 offset:1024
	ds_read_b128 v[166:169], v140 offset:2048
	ds_read_b128 v[174:177], v140 offset:3072
	ds_read_b128 v[178:181], v138 offset:32768
	ds_read_b128 v[182:185], v138 offset:33792
	ds_read_b128 v[186:189], v138 offset:34816
	ds_read_b128 v[190:193], v138 offset:35840
	ds_read_b128 v[194:197], v138 offset:36864
	ds_read_b128 v[198:201], v138 offset:37888
	ds_read_b128 v[202:205], v138 offset:38912
	ds_read_b128 v[206:209], v138 offset:39936
	s_add_u32 s12, s20, 0x40000
	s_addc_u32 s13, s21, 0
	s_mov_b32 s20, m0
	s_mov_b32 m0, s31
	s_nop 2
	global_load_lds_dwordx4 v132, s[12:13]
	s_mov_b32 m0, s20
	s_nop 0
	s_mov_b32 s20, m0
	s_mov_b32 m0, s33
	s_nop 2
	global_load_lds_dwordx4 v134, s[12:13]
	s_mov_b32 m0, s20
	s_waitcnt vmcnt(8)
	s_waitcnt lgkmcnt(0)
	s_barrier
	s_setprio 1
	s_waitcnt lgkmcnt(7)
	v_mfma_f32_16x16x32_bf16 v[126:129], v[142:145], v[178:181], v[126:129]
	v_mfma_f32_16x16x32_bf16 v[122:125], v[150:153], v[178:181], v[122:125]
	s_waitcnt lgkmcnt(5)
	v_mfma_f32_16x16x32_bf16 v[110:113], v[142:145], v[186:189], v[110:113]
	v_mfma_f32_16x16x32_bf16 v[106:109], v[150:153], v[186:189], v[106:109]
	s_waitcnt lgkmcnt(3)
	v_mfma_f32_16x16x32_bf16 v[94:97], v[142:145], v[194:197], v[94:97]
	v_mfma_f32_16x16x32_bf16 v[90:93], v[150:153], v[194:197], v[90:93]
	s_waitcnt lgkmcnt(1)
	v_mfma_f32_16x16x32_bf16 v[78:81], v[142:145], v[202:205], v[78:81]
	v_mfma_f32_16x16x32_bf16 v[74:77], v[150:153], v[202:205], v[74:77]
	v_mfma_f32_16x16x32_bf16 v[126:129], v[146:149], v[182:185], v[126:129]
	v_mfma_f32_16x16x32_bf16 v[122:125], v[154:157], v[182:185], v[122:125]
	v_mfma_f32_16x16x32_bf16 v[110:113], v[146:149], v[190:193], v[110:113]
	v_mfma_f32_16x16x32_bf16 v[106:109], v[154:157], v[190:193], v[106:109]
	v_mfma_f32_16x16x32_bf16 v[94:97], v[146:149], v[198:201], v[94:97]
	v_mfma_f32_16x16x32_bf16 v[90:93], v[154:157], v[198:201], v[90:93]
	s_waitcnt lgkmcnt(0)
	v_mfma_f32_16x16x32_bf16 v[78:81], v[146:149], v[206:209], v[78:81]
	v_mfma_f32_16x16x32_bf16 v[74:77], v[154:157], v[206:209], v[74:77]
	s_setprio 0
	s_setprio 1
	v_mfma_f32_16x16x32_bf16 v[118:121], v[158:161], v[178:181], v[118:121]
	v_mfma_f32_16x16x32_bf16 v[114:117], v[166:169], v[178:181], v[114:117]
	v_mfma_f32_16x16x32_bf16 v[102:105], v[158:161], v[186:189], v[102:105]
	v_mfma_f32_16x16x32_bf16 v[98:101], v[166:169], v[186:189], v[98:101]
	v_mfma_f32_16x16x32_bf16 v[86:89], v[158:161], v[194:197], v[86:89]
	v_mfma_f32_16x16x32_bf16 v[82:85], v[166:169], v[194:197], v[82:85]
	v_mfma_f32_16x16x32_bf16 v[70:73], v[158:161], v[202:205], v[70:73]
	v_mfma_f32_16x16x32_bf16 v[66:69], v[166:169], v[202:205], v[66:69]
	v_mfma_f32_16x16x32_bf16 v[118:121], v[162:165], v[182:185], v[118:121]
	v_mfma_f32_16x16x32_bf16 v[114:117], v[174:177], v[182:185], v[114:117]
	v_mfma_f32_16x16x32_bf16 v[102:105], v[162:165], v[190:193], v[102:105]
	v_mfma_f32_16x16x32_bf16 v[98:101], v[174:177], v[190:193], v[98:101]
	v_mfma_f32_16x16x32_bf16 v[86:89], v[162:165], v[198:201], v[86:89]
	v_mfma_f32_16x16x32_bf16 v[82:85], v[174:177], v[198:201], v[82:85]
	v_mfma_f32_16x16x32_bf16 v[70:73], v[162:165], v[206:209], v[70:73]
	v_mfma_f32_16x16x32_bf16 v[66:69], v[174:177], v[206:209], v[66:69]
	s_setprio 0
	s_barrier
	ds_read_b128 v[178:181], v138 offset:49152
	ds_read_b128 v[182:185], v138 offset:50176
	ds_read_b128 v[186:189], v138 offset:51200
	ds_read_b128 v[190:193], v138 offset:52224
	ds_read_b128 v[194:197], v138 offset:53248
	ds_read_b128 v[198:201], v138 offset:54272
	ds_read_b128 v[202:205], v138 offset:55296
	ds_read_b128 v[206:209], v138 offset:56320
	s_add_u32 s12, s18, 0x80
	s_addc_u32 s13, s19, 0
	s_mov_b32 s20, m0
	s_mov_b32 m0, s34
	s_nop 2
	global_load_lds_dwordx4 v133, s[12:13]
	s_mov_b32 m0, s20
	s_nop 0
	s_mov_b32 s20, m0
	s_mov_b32 m0, s35
	s_nop 2
	global_load_lds_dwordx4 v135, s[12:13]
	s_mov_b32 m0, s20
	s_add_u32 s12, s18, 0x40080
	s_addc_u32 s13, s19, 0
	s_mov_b32 s18, m0
	s_mov_b32 m0, s40
	s_nop 2
	global_load_lds_dwordx4 v133, s[12:13]
	s_mov_b32 m0, s18
	s_nop 0
	s_mov_b32 s18, m0
	s_mov_b32 m0, s41
	s_nop 2
	global_load_lds_dwordx4 v135, s[12:13]
	s_mov_b32 m0, s18
	s_mov_b32 s12, m0
	s_mov_b32 m0, s36
	s_nop 2
	global_load_lds_dwordx4 v132, s[16:17]
	s_mov_b32 m0, s12
	s_nop 0
	s_mov_b32 s12, m0
	s_mov_b32 m0, s37
	s_nop 2
	global_load_lds_dwordx4 v134, s[16:17]
	s_mov_b32 m0, s12
	s_waitcnt vmcnt(8)
	s_waitcnt lgkmcnt(0)
	s_barrier
	s_setprio 1
	s_waitcnt lgkmcnt(7)
	v_mfma_f32_16x16x32_bf16 v[62:65], v[142:145], v[178:181], v[62:65]
	v_mfma_f32_16x16x32_bf16 v[58:61], v[150:153], v[178:181], v[58:61]
	s_waitcnt lgkmcnt(5)
	v_mfma_f32_16x16x32_bf16 v[46:49], v[142:145], v[186:189], v[46:49]
	v_mfma_f32_16x16x32_bf16 v[42:45], v[150:153], v[186:189], v[42:45]
	s_waitcnt lgkmcnt(3)
	v_mfma_f32_16x16x32_bf16 v[30:33], v[142:145], v[194:197], v[30:33]
	v_mfma_f32_16x16x32_bf16 v[26:29], v[150:153], v[194:197], v[26:29]
	s_waitcnt lgkmcnt(1)
	v_mfma_f32_16x16x32_bf16 v[14:17], v[142:145], v[202:205], v[14:17]
	v_mfma_f32_16x16x32_bf16 v[10:13], v[150:153], v[202:205], v[10:13]
	v_mfma_f32_16x16x32_bf16 v[62:65], v[146:149], v[182:185], v[62:65]
	v_mfma_f32_16x16x32_bf16 v[58:61], v[154:157], v[182:185], v[58:61]
	v_mfma_f32_16x16x32_bf16 v[46:49], v[146:149], v[190:193], v[46:49]
	v_mfma_f32_16x16x32_bf16 v[42:45], v[154:157], v[190:193], v[42:45]
	v_mfma_f32_16x16x32_bf16 v[30:33], v[146:149], v[198:201], v[30:33]
	v_mfma_f32_16x16x32_bf16 v[26:29], v[154:157], v[198:201], v[26:29]
	s_waitcnt lgkmcnt(0)
	v_mfma_f32_16x16x32_bf16 v[14:17], v[146:149], v[206:209], v[14:17]
	v_mfma_f32_16x16x32_bf16 v[10:13], v[154:157], v[206:209], v[10:13]
	s_setprio 0
	s_setprio 1
	v_mfma_f32_16x16x32_bf16 v[54:57], v[158:161], v[178:181], v[54:57]
	v_mfma_f32_16x16x32_bf16 v[50:53], v[166:169], v[178:181], v[50:53]
	v_mfma_f32_16x16x32_bf16 v[38:41], v[158:161], v[186:189], v[38:41]
	v_mfma_f32_16x16x32_bf16 v[34:37], v[166:169], v[186:189], v[34:37]
	v_mfma_f32_16x16x32_bf16 v[22:25], v[158:161], v[194:197], v[22:25]
	v_mfma_f32_16x16x32_bf16 v[18:21], v[166:169], v[194:197], v[18:21]
	v_mfma_f32_16x16x32_bf16 v[6:9], v[158:161], v[202:205], v[6:9]
	v_mfma_f32_16x16x32_bf16 v[2:5], v[166:169], v[202:205], v[2:5]
	v_mfma_f32_16x16x32_bf16 v[54:57], v[162:165], v[182:185], v[54:57]
	v_mfma_f32_16x16x32_bf16 v[50:53], v[174:177], v[182:185], v[50:53]
	v_mfma_f32_16x16x32_bf16 v[38:41], v[162:165], v[190:193], v[38:41]
	v_mfma_f32_16x16x32_bf16 v[34:37], v[174:177], v[190:193], v[34:37]
	v_mfma_f32_16x16x32_bf16 v[22:25], v[162:165], v[198:201], v[22:25]
	v_mfma_f32_16x16x32_bf16 v[18:21], v[174:177], v[198:201], v[18:21]
	v_mfma_f32_16x16x32_bf16 v[6:9], v[162:165], v[206:209], v[6:9]
	v_mfma_f32_16x16x32_bf16 v[2:5], v[174:177], v[206:209], v[2:5]
	s_setprio 0
	s_barrier
	s_add_i32 s56, s56, 2
	s_add_u32 s54, s54, 0x100
	s_addc_u32 s55, s55, 0
	s_cmp_gt_u32 s56, 13
	s_mov_b64 s[12:13], s[14:15]
	s_cbranch_scc0 .LBB0_170
	s_cmpk_lt_u32 s23, 0x100
	s_cbranch_scc0 .LBB0_173
	s_barrier

.LBB0_1045:
	s_mov_b32 s3, -2
	s_mov_b64 s[56:57], 0
	s_waitcnt vmcnt(11)
	s_waitcnt vmcnt(10)
	s_waitcnt vmcnt(0)
.Lpeel1046:
	ds_read_b128 v[136:139], v172
	ds_read_b128 v[140:143], v172 offset:1024
	ds_read_b128 v[144:147], v172 offset:2048
	ds_read_b128 v[148:151], v172 offset:3072
	ds_read_b128 v[152:155], v173
	ds_read_b128 v[156:159], v173 offset:1024
	ds_read_b128 v[160:163], v173 offset:2048
	ds_read_b128 v[178:181], v173 offset:3072
	s_add_u32 s25, s64, s56
	s_addc_u32 s33, s65, s57
	s_add_u32 s66, s25, 0x100
	s_addc_u32 s67, s33, 0
	s_add_u32 s23, s62, s56
	s_addc_u32 s24, s63, s57
	s_add_u32 s28, s23, 0x100
	s_addc_u32 s29, s24, 0
	s_add_u32 s58, s25, 0x180
	s_addc_u32 s59, s33, 0
	ds_read_b128 v[182:185], v174
	ds_read_b128 v[186:189], v174 offset:1024
	ds_read_b128 v[190:193], v174 offset:2048
	ds_read_b128 v[194:197], v174 offset:3072
	ds_read_b128 v[198:201], v174 offset:4096
	ds_read_b128 v[202:205], v174 offset:5120
	ds_read_b128 v[206:209], v174 offset:6144
	ds_read_b128 v[210:213], v174 offset:7168
	s_add_u32 s30, s25, 0x40080
	s_addc_u32 s31, s33, 0
	s_mov_b32 s36, m0
	s_mov_b32 m0, s26
	s_nop 2
	global_load_lds_dwordx4 v165, s[30:31]
	s_mov_b32 m0, s36
	s_nop 0
	s_mov_b32 s36, m0
	s_mov_b32 m0, s27
	s_nop 2
	global_load_lds_dwordx4 v167, s[30:31]
	s_mov_b32 m0, s36
	s_waitcnt vmcnt(8)
	s_waitcnt lgkmcnt(0)
	s_barrier
	s_setprio 1
	s_waitcnt lgkmcnt(7)
	v_mfma_f32_16x16x32_bf16 v[26:29], v[136:139], v[182:185], 0
	v_mfma_f32_16x16x32_bf16 v[30:33], v[144:147], v[182:185], 0
	s_waitcnt lgkmcnt(5)
	v_mfma_f32_16x16x32_bf16 v[50:53], v[136:139], v[190:193], 0
	v_mfma_f32_16x16x32_bf16 v[54:57], v[144:147], v[190:193], 0
	s_waitcnt lgkmcnt(3)
	v_mfma_f32_16x16x32_bf16 v[74:77], v[136:139], v[198:201], 0
	v_mfma_f32_16x16x32_bf16 v[78:81], v[144:147], v[198:201], 0
	s_waitcnt lgkmcnt(1)
	v_mfma_f32_16x16x32_bf16 v[94:97], v[136:139], v[206:209], 0
	v_mfma_f32_16x16x32_bf16 v[102:105], v[144:147], v[206:209], 0
	v_mfma_f32_16x16x32_bf16 v[26:29], v[140:143], v[186:189], v[26:29]
	v_mfma_f32_16x16x32_bf16 v[30:33], v[148:151], v[186:189], v[30:33]
	v_mfma_f32_16x16x32_bf16 v[50:53], v[140:143], v[194:197], v[50:53]
	v_mfma_f32_16x16x32_bf16 v[54:57], v[148:151], v[194:197], v[54:57]
	v_mfma_f32_16x16x32_bf16 v[74:77], v[140:143], v[202:205], v[74:77]
	v_mfma_f32_16x16x32_bf16 v[78:81], v[148:151], v[202:205], v[78:81]
	s_waitcnt lgkmcnt(0)
	v_mfma_f32_16x16x32_bf16 v[94:97], v[140:143], v[210:213], v[94:97]
	v_mfma_f32_16x16x32_bf16 v[102:105], v[148:151], v[210:213], v[102:105]
	s_setprio 0
	s_setprio 1
	v_mfma_f32_16x16x32_bf16 v[38:41], v[152:155], v[182:185], 0
	v_mfma_f32_16x16x32_bf16 v[42:45], v[160:163], v[182:185], 0
	v_mfma_f32_16x16x32_bf16 v[62:65], v[152:155], v[190:193], 0
	v_mfma_f32_16x16x32_bf16 v[66:69], v[160:163], v[190:193], 0
	v_mfma_f32_16x16x32_bf16 v[82:85], v[152:155], v[198:201], 0
	v_mfma_f32_16x16x32_bf16 v[90:93], v[160:163], v[198:201], 0
	v_mfma_f32_16x16x32_bf16 v[106:109], v[152:155], v[206:209], 0
	v_mfma_f32_16x16x32_bf16 v[114:117], v[160:163], v[206:209], 0
	v_mfma_f32_16x16x32_bf16 v[38:41], v[156:159], v[186:189], v[38:41]
	v_mfma_f32_16x16x32_bf16 v[42:45], v[178:181], v[186:189], v[42:45]
	v_mfma_f32_16x16x32_bf16 v[62:65], v[156:159], v[194:197], v[62:65]
	v_mfma_f32_16x16x32_bf16 v[66:69], v[178:181], v[194:197], v[66:69]
	v_mfma_f32_16x16x32_bf16 v[82:85], v[156:159], v[202:205], v[82:85]
	v_mfma_f32_16x16x32_bf16 v[90:93], v[178:181], v[202:205], v[90:93]
	v_mfma_f32_16x16x32_bf16 v[106:109], v[156:159], v[210:213], v[106:109]
	v_mfma_f32_16x16x32_bf16 v[114:117], v[178:181], v[210:213], v[114:117]
	s_setprio 0
	s_barrier
	ds_read_b128 v[182:185], v174 offset:16384
	ds_read_b128 v[186:189], v174 offset:17408
	ds_read_b128 v[190:193], v174 offset:18432
	ds_read_b128 v[194:197], v174 offset:19456
	ds_read_b128 v[198:201], v174 offset:20480
	ds_read_b128 v[202:205], v174 offset:21504
	ds_read_b128 v[206:209], v174 offset:22528
	ds_read_b128 v[210:213], v174 offset:23552
	s_mov_b32 s30, m0
	s_mov_b32 m0, s80
	s_nop 2
	global_load_lds_dwordx4 v166, s[28:29]
	s_mov_b32 m0, s30
	s_nop 0
	s_mov_b32 s30, m0
	s_mov_b32 m0, s81
	s_nop 2
	global_load_lds_dwordx4 v168, s[28:29]
	s_mov_b32 m0, s30
	s_add_u32 s28, s23, 0x40100
	s_addc_u32 s29, s24, 0
	s_mov_b32 s30, m0
	s_mov_b32 m0, s82
	s_nop 2
	global_load_lds_dwordx4 v166, s[28:29]
	s_mov_b32 m0, s30
	s_nop 0
	s_mov_b32 s30, m0
	s_mov_b32 m0, s83
	s_nop 2
	global_load_lds_dwordx4 v168, s[28:29]
	s_mov_b32 m0, s30
	s_mov_b32 s28, m0
	s_mov_b32 m0, s79
	s_nop 2
	global_load_lds_dwordx4 v165, s[66:67]
	s_mov_b32 m0, s28
	s_nop 0
	s_mov_b32 s28, m0
	s_mov_b32 m0, s84
	s_nop 2
	global_load_lds_dwordx4 v167, s[66:67]
	s_mov_b32 m0, s28
	s_waitcnt vmcnt(8)
	s_waitcnt lgkmcnt(0)
	s_barrier
	s_setprio 1
	s_waitcnt lgkmcnt(7)
	v_mfma_f32_16x16x32_bf16 v[118:121], v[136:139], v[182:185], 0
	v_mfma_f32_16x16x32_bf16 v[126:129], v[144:147], v[182:185], 0
	s_waitcnt lgkmcnt(5)
	v_mfma_f32_16x16x32_bf16 v[98:101], v[136:139], v[190:193], 0
	v_mfma_f32_16x16x32_bf16 v[86:89], v[144:147], v[190:193], 0
	s_waitcnt lgkmcnt(3)
	v_mfma_f32_16x16x32_bf16 v[46:49], v[136:139], v[198:201], 0
	v_mfma_f32_16x16x32_bf16 v[34:37], v[144:147], v[198:201], 0
	s_waitcnt lgkmcnt(1)
	v_mfma_f32_16x16x32_bf16 v[14:17], v[136:139], v[206:209], 0
	v_mfma_f32_16x16x32_bf16 v[10:13], v[144:147], v[206:209], 0
	v_mfma_f32_16x16x32_bf16 v[118:121], v[140:143], v[186:189], v[118:121]
	v_mfma_f32_16x16x32_bf16 v[126:129], v[148:151], v[186:189], v[126:129]
	v_mfma_f32_16x16x32_bf16 v[98:101], v[140:143], v[194:197], v[98:101]
	v_mfma_f32_16x16x32_bf16 v[86:89], v[148:151], v[194:197], v[86:89]
	v_mfma_f32_16x16x32_bf16 v[46:49], v[140:143], v[202:205], v[46:49]
	v_mfma_f32_16x16x32_bf16 v[34:37], v[148:151], v[202:205], v[34:37]
	s_waitcnt lgkmcnt(0)
	v_mfma_f32_16x16x32_bf16 v[14:17], v[140:143], v[210:213], v[14:17]
	v_mfma_f32_16x16x32_bf16 v[10:13], v[148:151], v[210:213], v[10:13]
	s_setprio 0
	s_setprio 1
	v_mfma_f32_16x16x32_bf16 v[122:125], v[152:155], v[182:185], 0
	v_mfma_f32_16x16x32_bf16 v[110:113], v[160:163], v[182:185], 0
	v_mfma_f32_16x16x32_bf16 v[70:73], v[152:155], v[190:193], 0
	v_mfma_f32_16x16x32_bf16 v[58:61], v[160:163], v[190:193], 0
	v_mfma_f32_16x16x32_bf16 v[22:25], v[152:155], v[198:201], 0
	v_mfma_f32_16x16x32_bf16 v[18:21], v[160:163], v[198:201], 0
	v_mfma_f32_16x16x32_bf16 v[6:9], v[152:155], v[206:209], 0
	v_mfma_f32_16x16x32_bf16 v[2:5], v[160:163], v[206:209], 0
	v_mfma_f32_16x16x32_bf16 v[122:125], v[156:159], v[186:189], v[122:125]
	v_mfma_f32_16x16x32_bf16 v[110:113], v[178:181], v[186:189], v[110:113]
	v_mfma_f32_16x16x32_bf16 v[70:73], v[156:159], v[194:197], v[70:73]
	v_mfma_f32_16x16x32_bf16 v[58:61], v[178:181], v[194:197], v[58:61]
	v_mfma_f32_16x16x32_bf16 v[22:25], v[156:159], v[202:205], v[22:25]
	v_mfma_f32_16x16x32_bf16 v[18:21], v[178:181], v[202:205], v[18:21]
	v_mfma_f32_16x16x32_bf16 v[6:9], v[156:159], v[210:213], v[6:9]
	v_mfma_f32_16x16x32_bf16 v[2:5], v[178:181], v[210:213], v[2:5]
	s_setprio 0
	s_barrier
	s_branch .Lmid1046

.Lmid1046:
	ds_read_b128 v[136:139], v175
	ds_read_b128 v[140:143], v175 offset:1024
	ds_read_b128 v[144:147], v175 offset:2048
	ds_read_b128 v[148:151], v175 offset:3072
	ds_read_b128 v[152:155], v176
	ds_read_b128 v[156:159], v176 offset:1024
	ds_read_b128 v[160:163], v176 offset:2048
	ds_read_b128 v[178:181], v176 offset:3072
	ds_read_b128 v[182:185], v174 offset:32768
	ds_read_b128 v[186:189], v174 offset:33792
	ds_read_b128 v[190:193], v174 offset:34816
	ds_read_b128 v[194:197], v174 offset:35840
	ds_read_b128 v[198:201], v174 offset:36864
	ds_read_b128 v[202:205], v174 offset:37888
	ds_read_b128 v[206:209], v174 offset:38912
	ds_read_b128 v[210:213], v174 offset:39936
	s_add_u32 s28, s25, 0x40100
	s_addc_u32 s29, s33, 0
	s_mov_b32 s25, m0
	s_mov_b32 m0, s85
	s_nop 2
	global_load_lds_dwordx4 v165, s[28:29]
	s_mov_b32 m0, s25
	s_nop 0
	s_mov_b32 s25, m0
	s_mov_b32 m0, s86
	s_nop 2
	global_load_lds_dwordx4 v167, s[28:29]
	s_mov_b32 m0, s25
	s_waitcnt vmcnt(8)
	s_waitcnt lgkmcnt(0)
	s_barrier
	s_setprio 1
	s_waitcnt lgkmcnt(7)
	v_mfma_f32_16x16x32_bf16 v[26:29], v[136:139], v[182:185], v[26:29]
	v_mfma_f32_16x16x32_bf16 v[30:33], v[144:147], v[182:185], v[30:33]
	s_waitcnt lgkmcnt(5)
	v_mfma_f32_16x16x32_bf16 v[50:53], v[136:139], v[190:193], v[50:53]
	v_mfma_f32_16x16x32_bf16 v[54:57], v[144:147], v[190:193], v[54:57]
	s_waitcnt lgkmcnt(3)
	v_mfma_f32_16x16x32_bf16 v[74:77], v[136:139], v[198:201], v[74:77]
	v_mfma_f32_16x16x32_bf16 v[78:81], v[144:147], v[198:201], v[78:81]
	s_waitcnt lgkmcnt(1)
	v_mfma_f32_16x16x32_bf16 v[94:97], v[136:139], v[206:209], v[94:97]
	v_mfma_f32_16x16x32_bf16 v[102:105], v[144:147], v[206:209], v[102:105]
	v_mfma_f32_16x16x32_bf16 v[26:29], v[140:143], v[186:189], v[26:29]
	v_mfma_f32_16x16x32_bf16 v[30:33], v[148:151], v[186:189], v[30:33]
	v_mfma_f32_16x16x32_bf16 v[50:53], v[140:143], v[194:197], v[50:53]
	v_mfma_f32_16x16x32_bf16 v[54:57], v[148:151], v[194:197], v[54:57]
	v_mfma_f32_16x16x32_bf16 v[74:77], v[140:143], v[202:205], v[74:77]
	v_mfma_f32_16x16x32_bf16 v[78:81], v[148:151], v[202:205], v[78:81]
	s_waitcnt lgkmcnt(0)
	v_mfma_f32_16x16x32_bf16 v[94:97], v[140:143], v[210:213], v[94:97]
	v_mfma_f32_16x16x32_bf16 v[102:105], v[148:151], v[210:213], v[102:105]
	s_setprio 0
	s_setprio 1
	v_mfma_f32_16x16x32_bf16 v[38:41], v[152:155], v[182:185], v[38:41]
	v_mfma_f32_16x16x32_bf16 v[42:45], v[160:163], v[182:185], v[42:45]
	v_mfma_f32_16x16x32_bf16 v[62:65], v[152:155], v[190:193], v[62:65]
	v_mfma_f32_16x16x32_bf16 v[66:69], v[160:163], v[190:193], v[66:69]
	v_mfma_f32_16x16x32_bf16 v[82:85], v[152:155], v[198:201], v[82:85]
	v_mfma_f32_16x16x32_bf16 v[90:93], v[160:163], v[198:201], v[90:93]
	v_mfma_f32_16x16x32_bf16 v[106:109], v[152:155], v[206:209], v[106:109]
	v_mfma_f32_16x16x32_bf16 v[114:117], v[160:163], v[206:209], v[114:117]
	v_mfma_f32_16x16x32_bf16 v[38:41], v[156:159], v[186:189], v[38:41]
	v_mfma_f32_16x16x32_bf16 v[42:45], v[178:181], v[186:189], v[42:45]
	v_mfma_f32_16x16x32_bf16 v[62:65], v[156:159], v[194:197], v[62:65]
	v_mfma_f32_16x16x32_bf16 v[66:69], v[178:181], v[194:197], v[66:69]
	v_mfma_f32_16x16x32_bf16 v[82:85], v[156:159], v[202:205], v[82:85]
	v_mfma_f32_16x16x32_bf16 v[90:93], v[178:181], v[202:205], v[90:93]
	v_mfma_f32_16x16x32_bf16 v[106:109], v[156:159], v[210:213], v[106:109]
	v_mfma_f32_16x16x32_bf16 v[114:117], v[178:181], v[210:213], v[114:117]
	s_setprio 0
	s_barrier
	ds_read_b128 v[182:185], v174 offset:49152
	ds_read_b128 v[186:189], v174 offset:50176
	ds_read_b128 v[190:193], v174 offset:51200
	ds_read_b128 v[194:197], v174 offset:52224
	ds_read_b128 v[198:201], v174 offset:53248
	ds_read_b128 v[202:205], v174 offset:54272
	ds_read_b128 v[206:209], v174 offset:55296
	ds_read_b128 v[210:213], v174 offset:56320
	s_add_u32 s28, s23, 0x180
	s_addc_u32 s29, s24, 0
	s_mov_b32 s25, m0
	s_mov_b32 m0, s92
	s_nop 2
	global_load_lds_dwordx4 v166, s[28:29]
	s_mov_b32 m0, s25
	s_nop 0
	s_mov_b32 s25, m0
	s_mov_b32 m0, s93
	s_nop 2
	global_load_lds_dwordx4 v168, s[28:29]
	s_mov_b32 m0, s25
	s_add_u32 s28, s23, 0x40180
	s_addc_u32 s29, s24, 0
	s_mov_b32 s23, m0
	s_mov_b32 m0, s96
	s_nop 2
	global_load_lds_dwordx4 v166, s[28:29]
	s_mov_b32 m0, s23
	s_nop 0
	s_mov_b32 s23, m0
	s_mov_b32 m0, s97
	s_nop 2
	global_load_lds_dwordx4 v168, s[28:29]
	s_mov_b32 m0, s23
	s_nop 0
	s_mov_b32 s23, m0
	s_mov_b32 m0, s94
	s_nop 2
	global_load_lds_dwordx4 v165, s[58:59]
	s_mov_b32 m0, s23
	s_nop 0
	s_mov_b32 s23, m0
	s_mov_b32 m0, s95
	s_nop 2
	global_load_lds_dwordx4 v167, s[58:59]
	s_mov_b32 m0, s23
	s_waitcnt vmcnt(8)
	s_waitcnt lgkmcnt(0)
	s_barrier
	s_setprio 1
	s_waitcnt lgkmcnt(7)
	v_mfma_f32_16x16x32_bf16 v[118:121], v[136:139], v[182:185], v[118:121]
	v_mfma_f32_16x16x32_bf16 v[126:129], v[144:147], v[182:185], v[126:129]
	s_waitcnt lgkmcnt(5)
	v_mfma_f32_16x16x32_bf16 v[98:101], v[136:139], v[190:193], v[98:101]
	v_mfma_f32_16x16x32_bf16 v[86:89], v[144:147], v[190:193], v[86:89]
	s_waitcnt lgkmcnt(3)
	v_mfma_f32_16x16x32_bf16 v[46:49], v[136:139], v[198:201], v[46:49]
	v_mfma_f32_16x16x32_bf16 v[34:37], v[144:147], v[198:201], v[34:37]
	s_waitcnt lgkmcnt(1)
	v_mfma_f32_16x16x32_bf16 v[14:17], v[136:139], v[206:209], v[14:17]
	v_mfma_f32_16x16x32_bf16 v[10:13], v[144:147], v[206:209], v[10:13]
	v_mfma_f32_16x16x32_bf16 v[118:121], v[140:143], v[186:189], v[118:121]
	v_mfma_f32_16x16x32_bf16 v[126:129], v[148:151], v[186:189], v[126:129]
	v_mfma_f32_16x16x32_bf16 v[98:101], v[140:143], v[194:197], v[98:101]
	v_mfma_f32_16x16x32_bf16 v[86:89], v[148:151], v[194:197], v[86:89]
	v_mfma_f32_16x16x32_bf16 v[46:49], v[140:143], v[202:205], v[46:49]
	v_mfma_f32_16x16x32_bf16 v[34:37], v[148:151], v[202:205], v[34:37]
	s_waitcnt lgkmcnt(0)
	v_mfma_f32_16x16x32_bf16 v[14:17], v[140:143], v[210:213], v[14:17]
	v_mfma_f32_16x16x32_bf16 v[10:13], v[148:151], v[210:213], v[10:13]
	s_setprio 0
	s_setprio 1
	v_mfma_f32_16x16x32_bf16 v[122:125], v[152:155], v[182:185], v[122:125]
	v_mfma_f32_16x16x32_bf16 v[110:113], v[160:163], v[182:185], v[110:113]
	v_mfma_f32_16x16x32_bf16 v[70:73], v[152:155], v[190:193], v[70:73]
	v_mfma_f32_16x16x32_bf16 v[58:61], v[160:163], v[190:193], v[58:61]
	v_mfma_f32_16x16x32_bf16 v[22:25], v[152:155], v[198:201], v[22:25]
	v_mfma_f32_16x16x32_bf16 v[18:21], v[160:163], v[198:201], v[18:21]
	v_mfma_f32_16x16x32_bf16 v[6:9], v[152:155], v[206:209], v[6:9]
	v_mfma_f32_16x16x32_bf16 v[2:5], v[160:163], v[206:209], v[2:5]
	v_mfma_f32_16x16x32_bf16 v[122:125], v[156:159], v[186:189], v[122:125]
	v_mfma_f32_16x16x32_bf16 v[110:113], v[178:181], v[186:189], v[110:113]
	v_mfma_f32_16x16x32_bf16 v[70:73], v[156:159], v[194:197], v[70:73]
	v_mfma_f32_16x16x32_bf16 v[58:61], v[178:181], v[194:197], v[58:61]
	v_mfma_f32_16x16x32_bf16 v[22:25], v[156:159], v[202:205], v[22:25]
	v_mfma_f32_16x16x32_bf16 v[18:21], v[178:181], v[202:205], v[18:21]
	v_mfma_f32_16x16x32_bf16 v[6:9], v[156:159], v[210:213], v[6:9]
	v_mfma_f32_16x16x32_bf16 v[2:5], v[178:181], v[210:213], v[2:5]
	s_setprio 0
	s_barrier
	s_add_i32 s3, s3, 2
	s_add_u32 s56, s56, 0x100
	s_addc_u32 s57, s57, 0
	s_cmp_gt_u32 s3, 5
	s_cbranch_scc0 .LBB0_1046
	s_ashr_i32 s55, s54, 31
	s_lshl_b64 s[24:25], s[54:55], 19
	s_add_u32 s56, s69, s24
	s_addc_u32 s57, s76, s25
	s_ashr_i32 s23, s22, 31
	s_lshl_b64 s[24:25], s[22:23], 19
	s_add_u32 s58, s77, s24
	s_addc_u32 s59, s78, s25
	s_lshl_b32 s3, s60, 18
	s_lshl_b32 s23, s2, 8
	s_add_i32 s2, s23, s3
	v_add_u32_e32 v134, s2, v171
	global_load_dwordx2 v[162:163], v134, s[14:15]
	global_load_dwordx2 v[178:179], v134, s[16:17]
	v_or_b32_e32 v136, 0x80, v134
	v_add_u32_e32 v137, 0x4000, v134
	v_add_u32_e32 v138, 0x4080, v134
	v_add_u32_e32 v139, 0x8000, v134
	v_add_u32_e32 v140, 0x8080, v134
	v_add_u32_e32 v141, 0xc000, v134
	v_add_u32_e32 v161, 0xc080, v134
	global_load_dwordx2 v[180:181], v136, s[14:15]
	global_load_dwordx2 v[182:183], v136, s[16:17]
	global_load_dwordx2 v[158:159], v137, s[14:15]
	global_load_dwordx2 v[156:157], v137, s[16:17]
	global_load_dwordx2 v[154:155], v138, s[14:15]
	global_load_dwordx2 v[152:153], v138, s[16:17]
	global_load_dwordx2 v[150:151], v139, s[14:15]
	global_load_dwordx2 v[148:149], v139, s[16:17]
	global_load_dwordx2 v[146:147], v140, s[14:15]
	global_load_dwordx2 v[144:145], v140, s[16:17]
	global_load_dwordx2 v[142:143], v141, s[14:15]
	s_nop 0
	global_load_dwordx2 v[140:141], v141, s[16:17]
	s_nop 0
	global_load_dwordx2 v[138:139], v161, s[14:15]
	global_load_dwordx2 v[136:137], v161, s[16:17]
	v_add_u32_e32 v160, 0x20000, v134
	s_and_b64 s[2:3], s[4:5], exec
	s_cselect_b32 s2, s57, s65
	s_cselect_b32 s3, s56, s64
	s_cselect_b32 s24, s59, s63
	s_cselect_b32 s25, s58, s62
	s_add_u32 s28, s64, 0x500
	s_addc_u32 s29, s65, 0
	s_add_u32 s30, s62, 0x500
	s_addc_u32 s31, s63, 0
	s_mov_b32 s33, 6
	s_waitcnt vmcnt(15)
	v_cvt_pk_f32_fp8_e32 v[184:185], v162
	s_waitcnt vmcnt(14)
	v_cvt_pk_f32_fp8_e32 v[190:191], v178
	v_cvt_pk_f32_fp8_e32 v[188:189], v163
	v_cvt_pk_f32_fp8_sdwa v[192:193], v178 src0_sel:WORD_1
	v_cvt_pk_f32_fp8_e32 v[194:195], v179
	v_max_f32_e32 v161, v190, v190
	v_max_f32_e32 v184, v184, v184
	v_max_f32_e32 v190, v191, v191
	v_max_f32_e32 v185, v185, v185
	v_max_f32_e32 v188, v188, v188
	v_med3_f32 v161, v161, s35, v177
	v_med3_f32 v184, v184, s35, v177
	v_max_f32_e32 v191, v192, v192
	v_max_f32_e32 v192, v193, v193
	v_max_f32_e32 v193, v194, v194
	v_max_f32_e32 v194, v195, v195
	v_max_f32_e32 v189, v189, v189
	v_med3_f32 v190, v190, s35, v177
	v_med3_f32 v185, v185, s35, v177
	v_med3_f32 v188, v188, s35, v177
	v_mul_f32_e32 v161, 0xbfb8aa3b, v161
	v_mul_f32_e32 v195, 0xbfb8aa3b, v184
	v_cvt_pk_f32_fp8_sdwa v[186:187], v162 src0_sel:WORD_1
	v_cvt_pk_f32_fp8_sdwa v[162:163], v163 src0_sel:WORD_1
	v_med3_f32 v194, v194, s35, v177
	v_med3_f32 v189, v189, s35, v177
	v_mul_f32_e32 v190, 0xbfb8aa3b, v190
	v_mul_f32_e32 v196, 0xbfb8aa3b, v185
	v_mul_f32_e32 v199, 0xbfb8aa3b, v188
	v_exp_f32_e32 v184, v161
	v_exp_f32_e32 v161, v195
	v_mul_f32_e32 v200, 0xbfb8aa3b, v194
	v_mul_f32_e32 v189, 0xbfb8aa3b, v189
	v_exp_f32_e32 v185, v190
	v_exp_f32_e32 v190, v196
	v_exp_f32_e32 v194, v199
	v_exp_f32_e32 v195, v189
	v_cvt_pk_f32_fp8_sdwa v[178:179], v179 src0_sel:WORD_1
	v_add_f32_e32 v161, 1.0, v161
	v_max_f32_e32 v162, v162, v162
	v_add_f32_e32 v189, 1.0, v190
	v_rcp_f32_e32 v190, v161
	v_add_f32_e32 v161, 1.0, v194
	v_med3_f32 v162, v162, s35, v177
	v_rcp_f32_e32 v194, v161
	v_add_f32_e32 v161, 1.0, v195
	v_mul_f32_e32 v162, 0xbfb8aa3b, v162
	v_rcp_f32_e32 v195, v161
	v_max_f32_e32 v161, v178, v178
	v_exp_f32_e32 v178, v162
	v_max_f32_e32 v163, v163, v163
	v_med3_f32 v161, v161, s35, v177
	v_med3_f32 v163, v163, s35, v177
	v_mul_f32_e32 v161, 0xbfb8aa3b, v161
	v_mul_f32_e32 v163, 0xbfb8aa3b, v163
	v_max_f32_e32 v186, v186, v186
	v_max_f32_e32 v187, v187, v187
	v_exp_f32_e32 v162, v161
	v_add_f32_e32 v161, 1.0, v178
	v_max_f32_e32 v178, v179, v179
	v_exp_f32_e32 v179, v163
	v_med3_f32 v191, v191, s35, v177
	v_med3_f32 v186, v186, s35, v177
	v_med3_f32 v192, v192, s35, v177
	v_med3_f32 v187, v187, s35, v177
	v_mul_f32_e32 v191, 0xbfb8aa3b, v191
	v_mul_f32_e32 v197, 0xbfb8aa3b, v186
	v_mul_f32_e32 v192, 0xbfb8aa3b, v192
	v_mul_f32_e32 v198, 0xbfb8aa3b, v187
	v_med3_f32 v178, v178, s35, v177
	v_exp_f32_e32 v186, v191
	v_exp_f32_e32 v191, v197
	v_exp_f32_e32 v187, v192
	v_exp_f32_e32 v192, v198
	v_mul_f32_e32 v163, 0xbfb8aa3b, v178
	v_exp_f32_e32 v163, v163
	v_rcp_f32_e32 v178, v161
	v_add_f32_e32 v161, 1.0, v179
	v_med3_f32 v193, v193, s35, v177
	v_rcp_f32_e32 v179, v161
	v_mul_f32_e32 v193, 0xbfb8aa3b, v193
	v_exp_f32_e32 v188, v193
	v_add_f32_e32 v193, 1.0, v191
	v_add_f32_e32 v196, 1.0, v192
	v_rcp_f32_e32 v192, v193
	v_rcp_f32_e32 v193, v196
	v_pk_add_f32 v[162:163], v[162:163], 1.0 op_sel_hi:[1,0]
	v_pk_add_f32 v[186:187], v[186:187], 1.0 op_sel_hi:[1,0]
	v_pk_mul_f32 v[162:163], v[178:179], v[162:163]
	v_pk_mul_f32 v[186:187], v[192:193], v[186:187]
	v_pk_mul_f32 v[32:33], v[32:33], v[162:163]
	s_waitcnt vmcnt(13)
	v_cvt_pk_f32_fp8_e32 v[162:163], v180
	v_pk_mul_f32 v[28:29], v[28:29], v[186:187]
	s_waitcnt vmcnt(12)
	v_cvt_pk_f32_fp8_e32 v[186:187], v182
	v_rcp_f32_e32 v191, v189
	v_max_f32_e32 v162, v162, v162
	v_med3_f32 v162, v162, s35, v177
	v_mul_f32_e32 v162, 0xbfb8aa3b, v162
	v_max_f32_e32 v161, v186, v186
	v_exp_f32_e32 v186, v162
	v_exp_f32_e32 v189, v200
	v_med3_f32 v161, v161, s35, v177
	v_max_f32_e32 v163, v163, v163
	v_cvt_pk_f32_fp8_sdwa v[178:179], v180 src0_sel:WORD_1
	v_mul_f32_e32 v161, 0xbfb8aa3b, v161
	v_med3_f32 v163, v163, s35, v177
	v_pk_add_f32 v[184:185], v[184:185], 1.0 op_sel_hi:[1,0]
	v_exp_f32_e32 v162, v161
	v_add_f32_e32 v161, 1.0, v186
	v_mul_f32_e32 v163, 0xbfb8aa3b, v163
	v_pk_mul_f32 v[184:185], v[190:191], v[184:185]
	v_rcp_f32_e32 v186, v161
	v_max_f32_e32 v161, v187, v187
	v_exp_f32_e32 v187, v163
	v_pk_mul_f32 v[26:27], v[26:27], v[184:185]
	v_pk_add_f32 v[184:185], v[188:189], 1.0 op_sel_hi:[1,0]
	v_cvt_pk_f32_fp8_sdwa v[188:189], v182 src0_sel:WORD_1
	v_med3_f32 v161, v161, s35, v177
	v_max_f32_e32 v178, v178, v178
	v_mul_f32_e32 v161, 0xbfb8aa3b, v161
	v_med3_f32 v178, v178, s35, v177
	v_exp_f32_e32 v163, v161
	v_add_f32_e32 v161, 1.0, v187
	v_mul_f32_e32 v178, 0xbfb8aa3b, v178
	v_pk_mul_f32 v[184:185], v[194:195], v[184:185]
	v_rcp_f32_e32 v187, v161
	v_max_f32_e32 v161, v188, v188
	v_exp_f32_e32 v188, v178
	v_pk_mul_f32 v[30:31], v[30:31], v[184:185]
	v_cvt_pk_f32_fp8_e32 v[184:185], v181
	v_max_f32_e32 v179, v179, v179
	v_med3_f32 v161, v161, s35, v177
	v_med3_f32 v179, v179, s35, v177
	v_mul_f32_e32 v161, 0xbfb8aa3b, v161
	v_mul_f32_e32 v179, 0xbfb8aa3b, v179
	v_pk_add_f32 v[162:163], v[162:163], 1.0 op_sel_hi:[1,0]
	v_exp_f32_e32 v178, v161
	v_add_f32_e32 v161, 1.0, v188
	v_max_f32_e32 v188, v189, v189
	v_exp_f32_e32 v189, v179
	v_pk_mul_f32 v[162:163], v[186:187], v[162:163]
	v_cvt_pk_f32_fp8_e32 v[190:191], v183
	v_pk_mul_f32 v[38:39], v[38:39], v[162:163]
	v_max_f32_e32 v162, v184, v184
	v_med3_f32 v162, v162, s35, v177
	v_med3_f32 v188, v188, s35, v177
	v_mul_f32_e32 v162, 0xbfb8aa3b, v162
	v_mul_f32_e32 v179, 0xbfb8aa3b, v188
	v_rcp_f32_e32 v188, v161
	v_add_f32_e32 v161, 1.0, v189
	v_exp_f32_e32 v163, v162
	v_exp_f32_e32 v179, v179
	v_rcp_f32_e32 v189, v161
	v_max_f32_e32 v161, v190, v190
	v_med3_f32 v161, v161, s35, v177
	v_mul_f32_e32 v161, 0xbfb8aa3b, v161
	v_exp_f32_e32 v162, v161
	v_add_f32_e32 v161, 1.0, v163
	v_max_f32_e32 v163, v185, v185
	v_cvt_pk_f32_fp8_sdwa v[180:181], v181 src0_sel:WORD_1
	v_pk_add_f32 v[178:179], v[178:179], 1.0 op_sel_hi:[1,0]
	v_med3_f32 v163, v163, s35, v177
	v_pk_mul_f32 v[178:179], v[188:189], v[178:179]
	v_mul_f32_e32 v163, 0xbfb8aa3b, v163
	v_pk_mul_f32 v[40:41], v[40:41], v[178:179]
	v_exp_f32_e32 v179, v163
	v_cvt_pk_f32_fp8_sdwa v[182:183], v183 src0_sel:WORD_1
	v_rcp_f32_e32 v178, v161
	v_max_f32_e32 v161, v191, v191
	v_med3_f32 v161, v161, s35, v177
	v_max_f32_e32 v180, v180, v180
	v_mul_f32_e32 v161, 0xbfb8aa3b, v161
	v_med3_f32 v180, v180, s35, v177
	v_exp_f32_e32 v163, v161
	v_add_f32_e32 v161, 1.0, v179
	v_mul_f32_e32 v180, 0xbfb8aa3b, v180
	v_rcp_f32_e32 v179, v161
	v_max_f32_e32 v161, v182, v182
	v_exp_f32_e32 v182, v180
	v_max_f32_e32 v181, v181, v181
	v_med3_f32 v161, v161, s35, v177
	v_med3_f32 v181, v181, s35, v177
	v_mul_f32_e32 v161, 0xbfb8aa3b, v161
	v_mul_f32_e32 v181, 0xbfb8aa3b, v181
	v_exp_f32_e32 v180, v161
	v_add_f32_e32 v161, 1.0, v182
	v_max_f32_e32 v182, v183, v183
	v_exp_f32_e32 v183, v181
	v_med3_f32 v182, v182, s35, v177
	v_mul_f32_e32 v181, 0xbfb8aa3b, v182
	v_exp_f32_e32 v181, v181
	v_rcp_f32_e32 v182, v161
	v_add_f32_e32 v161, 1.0, v183
	v_pk_add_f32 v[162:163], v[162:163], 1.0 op_sel_hi:[1,0]
	v_rcp_f32_e32 v183, v161
	v_pk_mul_f32 v[162:163], v[178:179], v[162:163]
	v_pk_add_f32 v[180:181], v[180:181], 1.0 op_sel_hi:[1,0]
	v_pk_mul_f32 v[42:43], v[42:43], v[162:163]
	s_waitcnt vmcnt(11)
	v_cvt_pk_f32_fp8_e32 v[162:163], v158
	v_pk_mul_f32 v[178:179], v[182:183], v[180:181]
	s_waitcnt vmcnt(10)
	v_cvt_pk_f32_fp8_e32 v[182:183], v156
	v_pk_mul_f32 v[44:45], v[44:45], v[178:179]
	v_max_f32_e32 v162, v162, v162
	v_med3_f32 v162, v162, s35, v177
	v_mul_f32_e32 v162, 0xbfb8aa3b, v162
	v_max_f32_e32 v161, v182, v182
	v_exp_f32_e32 v182, v162
	v_med3_f32 v161, v161, s35, v177
	v_max_f32_e32 v163, v163, v163
	v_cvt_pk_f32_fp8_sdwa v[178:179], v158 src0_sel:WORD_1
	v_mul_f32_e32 v161, 0xbfb8aa3b, v161
	v_med3_f32 v163, v163, s35, v177
	v_exp_f32_e32 v162, v161
	v_add_f32_e32 v161, 1.0, v182
	v_mul_f32_e32 v163, 0xbfb8aa3b, v163
	v_rcp_f32_e32 v182, v161
	v_max_f32_e32 v161, v183, v183
	v_exp_f32_e32 v183, v163
	v_cvt_pk_f32_fp8_sdwa v[184:185], v156 src0_sel:WORD_1
	v_med3_f32 v161, v161, s35, v177
	v_max_f32_e32 v178, v178, v178
	v_mul_f32_e32 v161, 0xbfb8aa3b, v161
	v_med3_f32 v178, v178, s35, v177
	v_exp_f32_e32 v163, v161
	v_add_f32_e32 v161, 1.0, v183
	v_mul_f32_e32 v178, 0xbfb8aa3b, v178
	v_rcp_f32_e32 v183, v161
	v_max_f32_e32 v161, v184, v184
	v_exp_f32_e32 v184, v178
	v_cvt_pk_f32_fp8_e32 v[180:181], v159
	v_max_f32_e32 v179, v179, v179
	v_med3_f32 v161, v161, s35, v177
	v_med3_f32 v179, v179, s35, v177
	v_mul_f32_e32 v161, 0xbfb8aa3b, v161
	v_mul_f32_e32 v179, 0xbfb8aa3b, v179
	v_pk_add_f32 v[162:163], v[162:163], 1.0 op_sel_hi:[1,0]
	v_cvt_pk_f32_fp8_sdwa v[158:159], v159 src0_sel:WORD_1
	v_exp_f32_e32 v178, v161
	v_add_f32_e32 v161, 1.0, v184
	v_max_f32_e32 v184, v185, v185
	v_exp_f32_e32 v185, v179
	v_pk_mul_f32 v[162:163], v[182:183], v[162:163]
	v_cvt_pk_f32_fp8_e32 v[186:187], v157
	v_pk_mul_f32 v[50:51], v[50:51], v[162:163]
	v_max_f32_e32 v162, v180, v180
	v_med3_f32 v162, v162, s35, v177
	v_med3_f32 v184, v184, s35, v177
	v_mul_f32_e32 v162, 0xbfb8aa3b, v162
	v_cvt_pk_f32_fp8_sdwa v[156:157], v157 src0_sel:WORD_1
	v_mul_f32_e32 v179, 0xbfb8aa3b, v184
	v_rcp_f32_e32 v184, v161
	v_add_f32_e32 v161, 1.0, v185
	v_exp_f32_e32 v163, v162
	v_max_f32_e32 v158, v158, v158
	v_max_f32_e32 v159, v159, v159
	v_exp_f32_e32 v179, v179
	v_rcp_f32_e32 v185, v161
	v_max_f32_e32 v161, v186, v186
	v_med3_f32 v158, v158, s35, v177
	v_med3_f32 v159, v159, s35, v177
	v_med3_f32 v161, v161, s35, v177
	v_mul_f32_e32 v158, 0xbfb8aa3b, v158
	v_mul_f32_e32 v159, 0xbfb8aa3b, v159
	v_mul_f32_e32 v161, 0xbfb8aa3b, v161
	v_exp_f32_e32 v158, v158
	v_exp_f32_e32 v159, v159
	v_exp_f32_e32 v162, v161
	v_add_f32_e32 v161, 1.0, v163
	v_max_f32_e32 v163, v181, v181
	v_max_f32_e32 v156, v156, v156
	v_max_f32_e32 v157, v157, v157
	v_pk_add_f32 v[178:179], v[178:179], 1.0 op_sel_hi:[1,0]
	v_med3_f32 v163, v163, s35, v177
	v_med3_f32 v156, v156, s35, v177
	v_med3_f32 v157, v157, s35, v177
	v_pk_mul_f32 v[178:179], v[184:185], v[178:179]
	v_mul_f32_e32 v163, 0xbfb8aa3b, v163
	v_mul_f32_e32 v156, 0xbfb8aa3b, v156
	v_mul_f32_e32 v157, 0xbfb8aa3b, v157
	v_pk_mul_f32 v[52:53], v[52:53], v[178:179]
	v_exp_f32_e32 v179, v163
	v_exp_f32_e32 v156, v156
	v_add_f32_e32 v158, 1.0, v158
	v_exp_f32_e32 v157, v157
	v_add_f32_e32 v159, 1.0, v159
	v_rcp_f32_e32 v178, v161
	v_max_f32_e32 v161, v187, v187
	v_rcp_f32_e32 v158, v158
	v_rcp_f32_e32 v159, v159
	v_med3_f32 v161, v161, s35, v177
	v_mul_f32_e32 v161, 0xbfb8aa3b, v161
	v_exp_f32_e32 v163, v161
	v_add_f32_e32 v161, 1.0, v179
	v_pk_add_f32 v[156:157], v[156:157], 1.0 op_sel_hi:[1,0]
	v_rcp_f32_e32 v179, v161
	v_pk_mul_f32 v[156:157], v[158:159], v[156:157]
	v_pk_add_f32 v[162:163], v[162:163], 1.0 op_sel_hi:[1,0]
	v_pk_mul_f32 v[56:57], v[56:57], v[156:157]
	s_waitcnt vmcnt(9)
	v_cvt_pk_f32_fp8_e32 v[156:157], v154
	v_pk_mul_f32 v[162:163], v[178:179], v[162:163]
	s_waitcnt vmcnt(8)
	v_cvt_pk_f32_fp8_e32 v[178:179], v152
	v_cvt_pk_f32_fp8_sdwa v[158:159], v154 src0_sel:WORD_1
	v_max_f32_e32 v156, v156, v156
	v_med3_f32 v156, v156, s35, v177
	v_mul_f32_e32 v156, 0xbfb8aa3b, v156
	v_max_f32_e32 v161, v178, v178
	v_exp_f32_e32 v178, v156
	v_max_f32_e32 v157, v157, v157
	v_med3_f32 v157, v157, s35, v177
	v_med3_f32 v156, v161, s35, v177
	v_add_f32_e32 v161, 1.0, v178
	v_mul_f32_e32 v157, 0xbfb8aa3b, v157
	v_rcp_f32_e32 v178, v161
	v_max_f32_e32 v161, v179, v179
	v_exp_f32_e32 v179, v157
	v_cvt_pk_f32_fp8_sdwa v[180:181], v152 src0_sel:WORD_1
	v_max_f32_e32 v158, v158, v158
	v_med3_f32 v158, v158, s35, v177
	v_med3_f32 v157, v161, s35, v177
	v_add_f32_e32 v161, 1.0, v179
	v_mul_f32_e32 v158, 0xbfb8aa3b, v158
	v_rcp_f32_e32 v179, v161
	v_max_f32_e32 v161, v180, v180
	v_exp_f32_e32 v180, v158
	v_max_f32_e32 v159, v159, v159
	v_med3_f32 v159, v159, s35, v177
	v_pk_mul_f32 v[54:55], v[54:55], v[162:163]
	v_cvt_pk_f32_fp8_e32 v[162:163], v155
	v_cvt_pk_f32_fp8_sdwa v[154:155], v155 src0_sel:WORD_1
	v_mul_f32_e32 v156, 0xbfb8aa3b, v156
	v_mul_f32_e32 v157, 0xbfb8aa3b, v157
	v_mul_f32_e32 v159, 0xbfb8aa3b, v159
	v_exp_f32_e32 v156, v156
	v_exp_f32_e32 v157, v157
	v_med3_f32 v158, v161, s35, v177
	v_add_f32_e32 v161, 1.0, v180
	v_max_f32_e32 v180, v181, v181
	v_exp_f32_e32 v181, v159
	v_med3_f32 v180, v180, s35, v177
	v_cvt_pk_f32_fp8_e32 v[182:183], v153
	v_cvt_pk_f32_fp8_sdwa v[152:153], v153 src0_sel:WORD_1
	v_mul_f32_e32 v158, 0xbfb8aa3b, v158
	v_mul_f32_e32 v159, 0xbfb8aa3b, v180
	v_max_f32_e32 v154, v154, v154
	v_max_f32_e32 v155, v155, v155
	v_exp_f32_e32 v158, v158
	v_exp_f32_e32 v159, v159
	v_rcp_f32_e32 v180, v161
	v_add_f32_e32 v161, 1.0, v181
	v_pk_add_f32 v[156:157], v[156:157], 1.0 op_sel_hi:[1,0]
	v_med3_f32 v154, v154, s35, v177
	v_med3_f32 v155, v155, s35, v177
	v_rcp_f32_e32 v181, v161
	v_pk_mul_f32 v[156:157], v[178:179], v[156:157]
	v_mul_f32_e32 v154, 0xbfb8aa3b, v154
	v_mul_f32_e32 v155, 0xbfb8aa3b, v155
	v_pk_mul_f32 v[62:63], v[62:63], v[156:157]
	v_max_f32_e32 v157, v162, v162
	v_exp_f32_e32 v154, v154
	v_exp_f32_e32 v155, v155
	v_med3_f32 v157, v157, s35, v177
	v_max_f32_e32 v152, v152, v152
	v_max_f32_e32 v153, v153, v153
	v_pk_add_f32 v[158:159], v[158:159], 1.0 op_sel_hi:[1,0]
	v_mul_f32_e32 v157, 0xbfb8aa3b, v157
	v_med3_f32 v152, v152, s35, v177
	v_med3_f32 v153, v153, s35, v177
	v_pk_mul_f32 v[158:159], v[180:181], v[158:159]
	v_exp_f32_e32 v157, v157
	v_mul_f32_e32 v152, 0xbfb8aa3b, v152
	v_mul_f32_e32 v153, 0xbfb8aa3b, v153
	v_pk_mul_f32 v[64:65], v[64:65], v[158:159]
	v_max_f32_e32 v159, v163, v163
	v_exp_f32_e32 v152, v152
	v_add_f32_e32 v154, 1.0, v154
	v_exp_f32_e32 v153, v153
	v_add_f32_e32 v155, 1.0, v155
	v_med3_f32 v159, v159, s35, v177
	v_rcp_f32_e32 v154, v154
	v_rcp_f32_e32 v155, v155
	v_mul_f32_e32 v159, 0xbfb8aa3b, v159
	v_add_f32_e32 v157, 1.0, v157
	v_exp_f32_e32 v159, v159
	v_max_f32_e32 v156, v182, v182
	v_rcp_f32_e32 v158, v157
	v_max_f32_e32 v157, v183, v183
	v_pk_add_f32 v[152:153], v[152:153], 1.0 op_sel_hi:[1,0]
	v_med3_f32 v156, v156, s35, v177
	v_med3_f32 v157, v157, s35, v177
	v_pk_mul_f32 v[152:153], v[154:155], v[152:153]
	v_mul_f32_e32 v156, 0xbfb8aa3b, v156
	v_mul_f32_e32 v157, 0xbfb8aa3b, v157
	v_pk_mul_f32 v[68:69], v[68:69], v[152:153]
	s_waitcnt vmcnt(7)
	v_cvt_pk_f32_fp8_e32 v[152:153], v150
	v_exp_f32_e32 v156, v156
	v_exp_f32_e32 v157, v157
	v_add_f32_e32 v159, 1.0, v159
	v_rcp_f32_e32 v159, v159
	v_max_f32_e32 v152, v152, v152
	v_pk_add_f32 v[156:157], v[156:157], 1.0 op_sel_hi:[1,0]
	v_med3_f32 v152, v152, s35, v177
	v_pk_mul_f32 v[156:157], v[158:159], v[156:157]
	s_waitcnt vmcnt(6)
	v_cvt_pk_f32_fp8_e32 v[158:159], v148
	v_mul_f32_e32 v152, 0xbfb8aa3b, v152
	v_exp_f32_e32 v161, v152
	v_cvt_pk_f32_fp8_sdwa v[154:155], v150 src0_sel:WORD_1
	v_max_f32_e32 v153, v153, v153
	v_med3_f32 v153, v153, s35, v177
	v_max_f32_e32 v158, v158, v158
	v_mul_f32_e32 v153, 0xbfb8aa3b, v153
	v_cvt_pk_f32_fp8_sdwa v[162:163], v148 src0_sel:WORD_1
	v_med3_f32 v152, v158, s35, v177
	v_add_f32_e32 v158, 1.0, v161
	v_exp_f32_e32 v161, v153
	v_max_f32_e32 v154, v154, v154
	v_med3_f32 v154, v154, s35, v177
	v_max_f32_e32 v159, v159, v159
	v_mul_f32_e32 v154, 0xbfb8aa3b, v154
	v_med3_f32 v153, v159, s35, v177
	v_add_f32_e32 v159, 1.0, v161
	v_max_f32_e32 v161, v162, v162
	v_exp_f32_e32 v162, v154
	v_max_f32_e32 v155, v155, v155
	v_med3_f32 v155, v155, s35, v177
	v_pk_mul_f32 v[66:67], v[66:67], v[156:157]
	v_cvt_pk_f32_fp8_e32 v[156:157], v151
	v_cvt_pk_f32_fp8_sdwa v[150:151], v151 src0_sel:WORD_1
	v_mul_f32_e32 v152, 0xbfb8aa3b, v152
	v_mul_f32_e32 v153, 0xbfb8aa3b, v153
	v_mul_f32_e32 v155, 0xbfb8aa3b, v155
	v_exp_f32_e32 v152, v152
	v_exp_f32_e32 v153, v153
	v_med3_f32 v154, v161, s35, v177
	v_add_f32_e32 v161, 1.0, v162
	v_max_f32_e32 v162, v163, v163
	v_exp_f32_e32 v163, v155
	v_rcp_f32_e32 v158, v158
	v_rcp_f32_e32 v159, v159
	v_med3_f32 v162, v162, s35, v177
	v_cvt_pk_f32_fp8_e32 v[178:179], v149
	v_cvt_pk_f32_fp8_sdwa v[148:149], v149 src0_sel:WORD_1
	v_mul_f32_e32 v154, 0xbfb8aa3b, v154
	v_mul_f32_e32 v155, 0xbfb8aa3b, v162
	v_max_f32_e32 v150, v150, v150
	v_max_f32_e32 v151, v151, v151
	v_exp_f32_e32 v154, v154
	v_exp_f32_e32 v155, v155
	v_rcp_f32_e32 v162, v161
	v_add_f32_e32 v161, 1.0, v163
	v_pk_add_f32 v[152:153], v[152:153], 1.0 op_sel_hi:[1,0]
	v_med3_f32 v150, v150, s35, v177
	v_med3_f32 v151, v151, s35, v177
	v_rcp_f32_e32 v163, v161
	v_pk_mul_f32 v[152:153], v[158:159], v[152:153]
	v_mul_f32_e32 v150, 0xbfb8aa3b, v150
	v_mul_f32_e32 v151, 0xbfb8aa3b, v151
	v_pk_mul_f32 v[74:75], v[74:75], v[152:153]
	v_max_f32_e32 v153, v156, v156
	v_exp_f32_e32 v150, v150
	v_exp_f32_e32 v151, v151
	v_med3_f32 v153, v153, s35, v177
	v_max_f32_e32 v148, v148, v148
	v_max_f32_e32 v149, v149, v149
	v_pk_add_f32 v[154:155], v[154:155], 1.0 op_sel_hi:[1,0]
	v_mul_f32_e32 v153, 0xbfb8aa3b, v153
	v_med3_f32 v148, v148, s35, v177
	v_med3_f32 v149, v149, s35, v177
	v_pk_mul_f32 v[154:155], v[162:163], v[154:155]
	v_exp_f32_e32 v153, v153
	v_mul_f32_e32 v148, 0xbfb8aa3b, v148
	v_mul_f32_e32 v149, 0xbfb8aa3b, v149
	v_pk_mul_f32 v[76:77], v[76:77], v[154:155]
	v_max_f32_e32 v155, v157, v157
	v_exp_f32_e32 v148, v148
	v_add_f32_e32 v150, 1.0, v150
	v_exp_f32_e32 v149, v149
	v_add_f32_e32 v151, 1.0, v151
	v_med3_f32 v155, v155, s35, v177
	v_rcp_f32_e32 v150, v150
	v_rcp_f32_e32 v151, v151
	v_mul_f32_e32 v155, 0xbfb8aa3b, v155
	v_add_f32_e32 v153, 1.0, v153
	v_exp_f32_e32 v155, v155
	v_max_f32_e32 v152, v178, v178
	v_rcp_f32_e32 v154, v153
	v_max_f32_e32 v153, v179, v179
	v_pk_add_f32 v[148:149], v[148:149], 1.0 op_sel_hi:[1,0]
	v_med3_f32 v152, v152, s35, v177
	v_med3_f32 v153, v153, s35, v177
	v_pk_mul_f32 v[148:149], v[150:151], v[148:149]
	v_mul_f32_e32 v152, 0xbfb8aa3b, v152
	v_mul_f32_e32 v153, 0xbfb8aa3b, v153
	v_pk_mul_f32 v[80:81], v[80:81], v[148:149]
	s_waitcnt vmcnt(5)
	v_cvt_pk_f32_fp8_e32 v[148:149], v146
	v_exp_f32_e32 v152, v152
	v_exp_f32_e32 v153, v153
	v_add_f32_e32 v155, 1.0, v155
	v_rcp_f32_e32 v155, v155
	v_max_f32_e32 v148, v148, v148
	v_pk_add_f32 v[152:153], v[152:153], 1.0 op_sel_hi:[1,0]
	v_med3_f32 v148, v148, s35, v177
	v_pk_mul_f32 v[152:153], v[154:155], v[152:153]
	s_waitcnt vmcnt(4)
	v_cvt_pk_f32_fp8_e32 v[154:155], v144
	v_mul_f32_e32 v148, 0xbfb8aa3b, v148
	v_exp_f32_e32 v161, v148
	v_cvt_pk_f32_fp8_sdwa v[150:151], v146 src0_sel:WORD_1
	v_max_f32_e32 v149, v149, v149
	v_med3_f32 v149, v149, s35, v177
	v_max_f32_e32 v154, v154, v154
	v_mul_f32_e32 v149, 0xbfb8aa3b, v149
	v_med3_f32 v148, v154, s35, v177
	v_add_f32_e32 v154, 1.0, v161
	v_exp_f32_e32 v161, v149
	v_max_f32_e32 v150, v150, v150
	v_med3_f32 v150, v150, s35, v177
	v_cvt_pk_f32_fp8_sdwa v[156:157], v144 src0_sel:WORD_1
	v_max_f32_e32 v155, v155, v155
	v_mul_f32_e32 v150, 0xbfb8aa3b, v150
	v_med3_f32 v149, v155, s35, v177
	v_add_f32_e32 v155, 1.0, v161
	v_exp_f32_e32 v161, v150
	v_max_f32_e32 v151, v151, v151
	v_med3_f32 v151, v151, s35, v177
	v_pk_mul_f32 v[78:79], v[78:79], v[152:153]
	v_cvt_pk_f32_fp8_e32 v[152:153], v147
	v_cvt_pk_f32_fp8_sdwa v[146:147], v147 src0_sel:WORD_1
	v_mul_f32_e32 v148, 0xbfb8aa3b, v148
	v_mul_f32_e32 v149, 0xbfb8aa3b, v149
	v_max_f32_e32 v156, v156, v156
	v_mul_f32_e32 v151, 0xbfb8aa3b, v151
	v_exp_f32_e32 v148, v148
	v_exp_f32_e32 v149, v149
	v_med3_f32 v150, v156, s35, v177
	v_add_f32_e32 v156, 1.0, v161
	v_exp_f32_e32 v161, v151
	v_rcp_f32_e32 v154, v154
	v_rcp_f32_e32 v155, v155
	v_max_f32_e32 v157, v157, v157
	v_med3_f32 v157, v157, s35, v177
	v_cvt_pk_f32_fp8_e32 v[158:159], v145
	v_cvt_pk_f32_fp8_sdwa v[144:145], v145 src0_sel:WORD_1
	v_mul_f32_e32 v150, 0xbfb8aa3b, v150
	v_mul_f32_e32 v151, 0xbfb8aa3b, v157
	v_max_f32_e32 v146, v146, v146
	v_max_f32_e32 v147, v147, v147
	v_exp_f32_e32 v150, v150
	v_exp_f32_e32 v151, v151
	v_add_f32_e32 v157, 1.0, v161
	v_pk_add_f32 v[148:149], v[148:149], 1.0 op_sel_hi:[1,0]
	v_med3_f32 v146, v146, s35, v177
	v_med3_f32 v147, v147, s35, v177
	v_rcp_f32_e32 v156, v156
	v_rcp_f32_e32 v157, v157
	v_pk_mul_f32 v[148:149], v[154:155], v[148:149]
	v_mul_f32_e32 v146, 0xbfb8aa3b, v146
	v_mul_f32_e32 v147, 0xbfb8aa3b, v147
	v_pk_mul_f32 v[82:83], v[82:83], v[148:149]
	v_max_f32_e32 v149, v152, v152
	v_exp_f32_e32 v146, v146
	v_exp_f32_e32 v147, v147
	v_med3_f32 v149, v149, s35, v177
	v_max_f32_e32 v144, v144, v144
	v_max_f32_e32 v145, v145, v145
	v_pk_add_f32 v[150:151], v[150:151], 1.0 op_sel_hi:[1,0]
	v_mul_f32_e32 v149, 0xbfb8aa3b, v149
	v_med3_f32 v144, v144, s35, v177
	v_med3_f32 v145, v145, s35, v177
	v_pk_mul_f32 v[150:151], v[156:157], v[150:151]
	v_exp_f32_e32 v149, v149
	v_mul_f32_e32 v144, 0xbfb8aa3b, v144
	v_mul_f32_e32 v145, 0xbfb8aa3b, v145
	v_pk_mul_f32 v[84:85], v[84:85], v[150:151]
	v_max_f32_e32 v151, v153, v153
	v_exp_f32_e32 v144, v144
	v_add_f32_e32 v146, 1.0, v146
	v_exp_f32_e32 v145, v145
	v_add_f32_e32 v147, 1.0, v147
	v_med3_f32 v151, v151, s35, v177
	v_rcp_f32_e32 v146, v146
	v_rcp_f32_e32 v147, v147
	v_mul_f32_e32 v151, 0xbfb8aa3b, v151
	v_add_f32_e32 v149, 1.0, v149
	v_exp_f32_e32 v151, v151
	v_max_f32_e32 v148, v158, v158
	v_rcp_f32_e32 v150, v149
	v_max_f32_e32 v149, v159, v159
	v_pk_add_f32 v[144:145], v[144:145], 1.0 op_sel_hi:[1,0]
	v_med3_f32 v148, v148, s35, v177
	v_med3_f32 v149, v149, s35, v177
	v_pk_mul_f32 v[144:145], v[146:147], v[144:145]
	v_mul_f32_e32 v148, 0xbfb8aa3b, v148
	v_mul_f32_e32 v149, 0xbfb8aa3b, v149
	v_pk_mul_f32 v[92:93], v[92:93], v[144:145]
	s_waitcnt vmcnt(3)
	v_cvt_pk_f32_fp8_e32 v[144:145], v142
	v_exp_f32_e32 v148, v148
	v_exp_f32_e32 v149, v149
	v_add_f32_e32 v151, 1.0, v151
	v_rcp_f32_e32 v151, v151
	v_max_f32_e32 v144, v144, v144
	v_pk_add_f32 v[148:149], v[148:149], 1.0 op_sel_hi:[1,0]
	v_med3_f32 v144, v144, s35, v177
	v_pk_mul_f32 v[148:149], v[150:151], v[148:149]
	s_waitcnt vmcnt(2)
	v_cvt_pk_f32_fp8_e32 v[150:151], v140
	v_mul_f32_e32 v144, 0xbfb8aa3b, v144
	v_exp_f32_e32 v156, v144
	v_cvt_pk_f32_fp8_sdwa v[146:147], v142 src0_sel:WORD_1
	v_max_f32_e32 v145, v145, v145
	v_med3_f32 v145, v145, s35, v177
	v_max_f32_e32 v150, v150, v150
	v_mul_f32_e32 v145, 0xbfb8aa3b, v145
	v_med3_f32 v144, v150, s35, v177
	v_add_f32_e32 v150, 1.0, v156
	v_exp_f32_e32 v156, v145
	v_max_f32_e32 v146, v146, v146
	v_med3_f32 v146, v146, s35, v177
	v_cvt_pk_f32_fp8_sdwa v[152:153], v140 src0_sel:WORD_1
	v_max_f32_e32 v151, v151, v151
	v_mul_f32_e32 v146, 0xbfb8aa3b, v146
	v_med3_f32 v145, v151, s35, v177
	v_add_f32_e32 v151, 1.0, v156
	v_exp_f32_e32 v156, v146
	v_max_f32_e32 v147, v147, v147
	v_med3_f32 v147, v147, s35, v177
	v_pk_mul_f32 v[90:91], v[90:91], v[148:149]
	v_cvt_pk_f32_fp8_e32 v[148:149], v143
	v_cvt_pk_f32_fp8_sdwa v[142:143], v143 src0_sel:WORD_1
	v_mul_f32_e32 v144, 0xbfb8aa3b, v144
	v_mul_f32_e32 v145, 0xbfb8aa3b, v145
	v_max_f32_e32 v152, v152, v152
	v_mul_f32_e32 v147, 0xbfb8aa3b, v147
	v_exp_f32_e32 v144, v144
	v_exp_f32_e32 v145, v145
	v_med3_f32 v146, v152, s35, v177
	v_add_f32_e32 v152, 1.0, v156
	v_exp_f32_e32 v156, v147
	v_rcp_f32_e32 v150, v150
	v_rcp_f32_e32 v151, v151
	v_max_f32_e32 v153, v153, v153
	v_med3_f32 v153, v153, s35, v177
	v_cvt_pk_f32_fp8_e32 v[154:155], v141
	v_cvt_pk_f32_fp8_sdwa v[140:141], v141 src0_sel:WORD_1
	v_mul_f32_e32 v146, 0xbfb8aa3b, v146
	v_mul_f32_e32 v147, 0xbfb8aa3b, v153
	v_max_f32_e32 v142, v142, v142
	v_max_f32_e32 v143, v143, v143
	v_exp_f32_e32 v146, v146
	v_exp_f32_e32 v147, v147
	v_add_f32_e32 v153, 1.0, v156
	v_pk_add_f32 v[144:145], v[144:145], 1.0 op_sel_hi:[1,0]
	v_med3_f32 v142, v142, s35, v177
	v_med3_f32 v143, v143, s35, v177
	v_rcp_f32_e32 v152, v152
	v_rcp_f32_e32 v153, v153
	v_pk_mul_f32 v[144:145], v[150:151], v[144:145]
	v_mul_f32_e32 v142, 0xbfb8aa3b, v142
	v_mul_f32_e32 v143, 0xbfb8aa3b, v143
	v_pk_mul_f32 v[94:95], v[94:95], v[144:145]
	v_max_f32_e32 v145, v148, v148
	v_exp_f32_e32 v142, v142
	v_exp_f32_e32 v143, v143
	v_med3_f32 v145, v145, s35, v177
	v_max_f32_e32 v140, v140, v140
	v_max_f32_e32 v141, v141, v141
	v_pk_add_f32 v[146:147], v[146:147], 1.0 op_sel_hi:[1,0]
	v_mul_f32_e32 v145, 0xbfb8aa3b, v145
	v_med3_f32 v140, v140, s35, v177
	v_med3_f32 v141, v141, s35, v177
	v_pk_mul_f32 v[146:147], v[152:153], v[146:147]
	v_exp_f32_e32 v145, v145
	v_mul_f32_e32 v140, 0xbfb8aa3b, v140
	v_mul_f32_e32 v141, 0xbfb8aa3b, v141
	v_pk_mul_f32 v[96:97], v[96:97], v[146:147]
	v_max_f32_e32 v147, v149, v149
	v_exp_f32_e32 v140, v140
	v_add_f32_e32 v142, 1.0, v142
	v_exp_f32_e32 v141, v141
	v_add_f32_e32 v143, 1.0, v143
	v_med3_f32 v147, v147, s35, v177
	v_rcp_f32_e32 v142, v142
	v_rcp_f32_e32 v143, v143
	v_mul_f32_e32 v147, 0xbfb8aa3b, v147
	v_add_f32_e32 v145, 1.0, v145
	v_exp_f32_e32 v147, v147
	v_max_f32_e32 v144, v154, v154
	v_rcp_f32_e32 v146, v145
	v_max_f32_e32 v145, v155, v155
	v_pk_add_f32 v[140:141], v[140:141], 1.0 op_sel_hi:[1,0]
	v_med3_f32 v144, v144, s35, v177
	v_med3_f32 v145, v145, s35, v177
	v_pk_mul_f32 v[140:141], v[142:143], v[140:141]
	v_mul_f32_e32 v144, 0xbfb8aa3b, v144
	v_mul_f32_e32 v145, 0xbfb8aa3b, v145
	v_pk_mul_f32 v[104:105], v[104:105], v[140:141]
	s_waitcnt vmcnt(1)
	v_cvt_pk_f32_fp8_e32 v[140:141], v138
	v_exp_f32_e32 v144, v144
	v_exp_f32_e32 v145, v145
	v_add_f32_e32 v147, 1.0, v147
	v_rcp_f32_e32 v147, v147
	v_max_f32_e32 v140, v140, v140
	v_pk_add_f32 v[144:145], v[144:145], 1.0 op_sel_hi:[1,0]
	v_med3_f32 v140, v140, s35, v177
	v_pk_mul_f32 v[144:145], v[146:147], v[144:145]
	s_waitcnt vmcnt(0)
	v_cvt_pk_f32_fp8_e32 v[146:147], v136
	v_mul_f32_e32 v140, 0xbfb8aa3b, v140
	v_exp_f32_e32 v152, v140
	v_cvt_pk_f32_fp8_sdwa v[142:143], v138 src0_sel:WORD_1
	v_max_f32_e32 v141, v141, v141
	v_med3_f32 v141, v141, s35, v177
	v_max_f32_e32 v146, v146, v146
	v_mul_f32_e32 v141, 0xbfb8aa3b, v141
	v_med3_f32 v140, v146, s35, v177
	v_add_f32_e32 v146, 1.0, v152
	v_exp_f32_e32 v152, v141
	v_max_f32_e32 v142, v142, v142
	v_med3_f32 v142, v142, s35, v177
	v_cvt_pk_f32_fp8_sdwa v[148:149], v136 src0_sel:WORD_1
	v_max_f32_e32 v147, v147, v147
	v_mul_f32_e32 v142, 0xbfb8aa3b, v142
	v_med3_f32 v141, v147, s35, v177
	v_add_f32_e32 v147, 1.0, v152
	v_exp_f32_e32 v152, v142
	v_max_f32_e32 v143, v143, v143
	v_med3_f32 v143, v143, s35, v177
	v_mul_f32_e32 v140, 0xbfb8aa3b, v140
	v_mul_f32_e32 v141, 0xbfb8aa3b, v141
	v_max_f32_e32 v148, v148, v148
	v_mul_f32_e32 v143, 0xbfb8aa3b, v143
	v_exp_f32_e32 v140, v140
	v_exp_f32_e32 v141, v141
	v_med3_f32 v142, v148, s35, v177
	v_add_f32_e32 v148, 1.0, v152
	v_exp_f32_e32 v152, v143
	v_rcp_f32_e32 v146, v146
	v_rcp_f32_e32 v147, v147
	v_max_f32_e32 v149, v149, v149
	v_pk_mul_f32 v[102:103], v[102:103], v[144:145]
	v_cvt_pk_f32_fp8_e32 v[144:145], v139
	v_med3_f32 v149, v149, s35, v177
	v_mul_f32_e32 v142, 0xbfb8aa3b, v142
	v_mul_f32_e32 v143, 0xbfb8aa3b, v149
	v_exp_f32_e32 v142, v142
	v_exp_f32_e32 v143, v143
	v_add_f32_e32 v149, 1.0, v152
	v_pk_add_f32 v[140:141], v[140:141], 1.0 op_sel_hi:[1,0]
	v_rcp_f32_e32 v148, v148
	v_rcp_f32_e32 v149, v149
	v_pk_mul_f32 v[140:141], v[146:147], v[140:141]
	v_cvt_pk_f32_fp8_sdwa v[138:139], v139 src0_sel:WORD_1
	v_pk_mul_f32 v[106:107], v[106:107], v[140:141]
	v_max_f32_e32 v141, v144, v144
	v_med3_f32 v141, v141, s35, v177
	v_pk_add_f32 v[142:143], v[142:143], 1.0 op_sel_hi:[1,0]
	v_mul_f32_e32 v141, 0xbfb8aa3b, v141
	v_pk_mul_f32 v[142:143], v[148:149], v[142:143]
	v_exp_f32_e32 v141, v141
	v_cvt_pk_f32_fp8_e32 v[150:151], v137
	v_cvt_pk_f32_fp8_sdwa v[136:137], v137 src0_sel:WORD_1
	v_pk_mul_f32 v[108:109], v[108:109], v[142:143]
	v_max_f32_e32 v143, v145, v145
	v_max_f32_e32 v138, v138, v138
	v_max_f32_e32 v139, v139, v139
	v_med3_f32 v143, v143, s35, v177
	v_med3_f32 v138, v138, s35, v177
	v_med3_f32 v139, v139, s35, v177
	v_mul_f32_e32 v143, 0xbfb8aa3b, v143
	v_mul_f32_e32 v138, 0xbfb8aa3b, v138
	v_mul_f32_e32 v139, 0xbfb8aa3b, v139
	v_add_f32_e32 v141, 1.0, v141
	v_exp_f32_e32 v143, v143
	v_exp_f32_e32 v138, v138
	v_exp_f32_e32 v139, v139
	v_max_f32_e32 v140, v150, v150
	v_rcp_f32_e32 v142, v141
	v_max_f32_e32 v141, v151, v151
	v_max_f32_e32 v136, v136, v136
	v_max_f32_e32 v137, v137, v137
	v_med3_f32 v140, v140, s35, v177
	v_med3_f32 v141, v141, s35, v177
	v_med3_f32 v136, v136, s35, v177
	v_med3_f32 v137, v137, s35, v177
	v_mul_f32_e32 v140, 0xbfb8aa3b, v140
	v_mul_f32_e32 v141, 0xbfb8aa3b, v141
	v_mul_f32_e32 v136, 0xbfb8aa3b, v136
	v_mul_f32_e32 v137, 0xbfb8aa3b, v137
	v_exp_f32_e32 v140, v140
	v_exp_f32_e32 v141, v141
	v_add_f32_e32 v143, 1.0, v143
	v_exp_f32_e32 v136, v136
	v_add_f32_e32 v138, 1.0, v138
	v_exp_f32_e32 v137, v137
	v_add_f32_e32 v139, 1.0, v139
	v_rcp_f32_e32 v143, v143
	v_rcp_f32_e32 v138, v138
	v_rcp_f32_e32 v139, v139
	v_pk_add_f32 v[136:137], v[136:137], 1.0 op_sel_hi:[1,0]
	v_pk_add_f32 v[140:141], v[140:141], 1.0 op_sel_hi:[1,0]
	v_pk_mul_f32 v[136:137], v[138:139], v[136:137]
	v_pk_mul_f32 v[140:141], v[142:143], v[140:141]
	v_pk_mul_f32 v[116:117], v[116:117], v[136:137]
	v_pk_mul_f32 v[114:115], v[114:115], v[140:141]
	s_nop 0
	global_load_dwordx2 v[162:163], v160, s[14:15]
	s_nop 0
	global_load_dwordx2 v[160:161], v160, s[16:17]
	v_add_u32_e32 v136, 0x20080, v134
	v_add_u32_e32 v137, 0x24000, v134
	v_add_u32_e32 v138, 0x24080, v134
	v_add_u32_e32 v139, 0x28000, v134
	v_add_u32_e32 v140, 0x28080, v134
	v_add_u32_e32 v141, 0x2c000, v134
	v_add_u32_e32 v134, 0x2c080, v134
	global_load_dwordx2 v[178:179], v136, s[14:15]
	global_load_dwordx2 v[180:181], v136, s[16:17]
	global_load_dwordx2 v[158:159], v137, s[14:15]
	global_load_dwordx2 v[156:157], v137, s[16:17]
	global_load_dwordx2 v[154:155], v138, s[14:15]
	global_load_dwordx2 v[152:153], v138, s[16:17]
	global_load_dwordx2 v[150:151], v139, s[14:15]
	global_load_dwordx2 v[148:149], v139, s[16:17]
	global_load_dwordx2 v[146:147], v140, s[14:15]
	global_load_dwordx2 v[144:145], v140, s[16:17]
	global_load_dwordx2 v[142:143], v141, s[14:15]
	s_nop 0
	global_load_dwordx2 v[140:141], v141, s[16:17]
	s_nop 0
	global_load_dwordx2 v[138:139], v134, s[14:15]
	global_load_dwordx2 v[136:137], v134, s[16:17]
	s_waitcnt vmcnt(15)
	v_cvt_pk_f32_fp8_e32 v[182:183], v162
	s_waitcnt vmcnt(14)
	v_cvt_pk_f32_fp8_e32 v[188:189], v160
	v_cvt_pk_f32_fp8_sdwa v[184:185], v162 src0_sel:WORD_1
	v_cvt_pk_f32_fp8_sdwa v[190:191], v160 src0_sel:WORD_1
	v_max_f32_e32 v182, v182, v182
	v_med3_f32 v182, v182, s35, v177
	v_mul_f32_e32 v182, 0xbfb8aa3b, v182
	v_max_f32_e32 v134, v188, v188
	v_exp_f32_e32 v188, v182
	v_med3_f32 v134, v134, s35, v177
	v_max_f32_e32 v183, v183, v183
	v_mul_f32_e32 v134, 0xbfb8aa3b, v134
	v_med3_f32 v183, v183, s35, v177
	v_exp_f32_e32 v182, v134
	v_add_f32_e32 v134, 1.0, v188
	v_mul_f32_e32 v183, 0xbfb8aa3b, v183
	v_rcp_f32_e32 v188, v134
	v_max_f32_e32 v134, v189, v189
	v_exp_f32_e32 v189, v183
	v_med3_f32 v134, v134, s35, v177
	v_max_f32_e32 v184, v184, v184
	v_mul_f32_e32 v134, 0xbfb8aa3b, v134
	v_med3_f32 v184, v184, s35, v177
	v_exp_f32_e32 v183, v134
	v_add_f32_e32 v134, 1.0, v189
	v_mul_f32_e32 v184, 0xbfb8aa3b, v184
	v_rcp_f32_e32 v189, v134
	v_max_f32_e32 v134, v190, v190
	v_exp_f32_e32 v190, v184
	v_cvt_pk_f32_fp8_e32 v[186:187], v163
	v_max_f32_e32 v185, v185, v185
	v_med3_f32 v134, v134, s35, v177
	v_med3_f32 v185, v185, s35, v177
	v_mul_f32_e32 v134, 0xbfb8aa3b, v134
	v_mul_f32_e32 v185, 0xbfb8aa3b, v185
	v_pk_add_f32 v[182:183], v[182:183], 1.0 op_sel_hi:[1,0]
	v_exp_f32_e32 v184, v134
	v_add_f32_e32 v134, 1.0, v190
	v_max_f32_e32 v190, v191, v191
	v_exp_f32_e32 v191, v185
	v_pk_mul_f32 v[182:183], v[188:189], v[182:183]
	v_cvt_pk_f32_fp8_e32 v[192:193], v161
	v_pk_mul_f32 v[118:119], v[118:119], v[182:183]
	v_max_f32_e32 v182, v186, v186
	v_med3_f32 v182, v182, s35, v177
	v_med3_f32 v190, v190, s35, v177
	v_mul_f32_e32 v182, 0xbfb8aa3b, v182
	v_mul_f32_e32 v185, 0xbfb8aa3b, v190
	v_rcp_f32_e32 v190, v134
	v_add_f32_e32 v134, 1.0, v191
	v_exp_f32_e32 v183, v182
	v_exp_f32_e32 v185, v185
	v_rcp_f32_e32 v191, v134
	v_max_f32_e32 v134, v192, v192
	v_med3_f32 v134, v134, s35, v177
	v_mul_f32_e32 v134, 0xbfb8aa3b, v134
	v_exp_f32_e32 v182, v134
	v_add_f32_e32 v134, 1.0, v183
	v_max_f32_e32 v183, v187, v187
	v_pk_add_f32 v[184:185], v[184:185], 1.0 op_sel_hi:[1,0]
	v_med3_f32 v183, v183, s35, v177
	v_pk_mul_f32 v[184:185], v[190:191], v[184:185]
	v_mul_f32_e32 v183, 0xbfb8aa3b, v183
	v_pk_mul_f32 v[120:121], v[120:121], v[184:185]
	v_exp_f32_e32 v185, v183
	v_cvt_pk_f32_fp8_sdwa v[162:163], v163 src0_sel:WORD_1
	v_cvt_pk_f32_fp8_sdwa v[160:161], v161 src0_sel:WORD_1
	v_rcp_f32_e32 v184, v134
	v_max_f32_e32 v134, v193, v193
	v_med3_f32 v134, v134, s35, v177
	v_mul_f32_e32 v134, 0xbfb8aa3b, v134
	v_exp_f32_e32 v183, v134
	v_add_f32_e32 v134, 1.0, v185
	v_rcp_f32_e32 v185, v134
	v_max_f32_e32 v134, v160, v160
	v_max_f32_e32 v160, v162, v162
	v_med3_f32 v160, v160, s35, v177
	v_mul_f32_e32 v160, 0xbfb8aa3b, v160
	v_exp_f32_e32 v162, v160
	v_med3_f32 v134, v134, s35, v177
	v_mul_f32_e32 v134, 0xbfb8aa3b, v134
	v_exp_f32_e32 v160, v134
	v_add_f32_e32 v134, 1.0, v162
	v_max_f32_e32 v162, v163, v163
	v_med3_f32 v162, v162, s35, v177
	v_mul_f32_e32 v162, 0xbfb8aa3b, v162
	v_exp_f32_e32 v163, v162
	v_max_f32_e32 v161, v161, v161
	v_med3_f32 v161, v161, s35, v177
	v_mul_f32_e32 v161, 0xbfb8aa3b, v161
	v_exp_f32_e32 v161, v161
	v_rcp_f32_e32 v162, v134
	v_add_f32_e32 v134, 1.0, v163
	v_rcp_f32_e32 v163, v134
	v_pk_add_f32 v[160:161], v[160:161], 1.0 op_sel_hi:[1,0]
	v_pk_add_f32 v[182:183], v[182:183], 1.0 op_sel_hi:[1,0]
	s_waitcnt vmcnt(12)
	v_cvt_pk_f32_fp8_sdwa v[186:187], v180 src0_sel:WORD_1
	v_pk_mul_f32 v[160:161], v[162:163], v[160:161]
	v_pk_mul_f32 v[182:183], v[184:185], v[182:183]
	v_pk_mul_f32 v[128:129], v[128:129], v[160:161]
	v_cvt_pk_f32_fp8_e32 v[160:161], v178
	v_cvt_pk_f32_fp8_e32 v[184:185], v180
	v_cvt_pk_f32_fp8_sdwa v[162:163], v178 src0_sel:WORD_1
	v_pk_mul_f32 v[126:127], v[126:127], v[182:183]
	v_max_f32_e32 v160, v160, v160
	v_med3_f32 v160, v160, s35, v177
	v_mul_f32_e32 v160, 0xbfb8aa3b, v160
	v_max_f32_e32 v134, v184, v184
	v_exp_f32_e32 v184, v160
	v_med3_f32 v134, v134, s35, v177
	v_max_f32_e32 v161, v161, v161
	v_mul_f32_e32 v134, 0xbfb8aa3b, v134
	v_med3_f32 v161, v161, s35, v177
	v_exp_f32_e32 v160, v134
	v_add_f32_e32 v134, 1.0, v184
	v_mul_f32_e32 v161, 0xbfb8aa3b, v161
	v_rcp_f32_e32 v184, v134
	v_max_f32_e32 v134, v185, v185
	v_exp_f32_e32 v185, v161
	v_med3_f32 v134, v134, s35, v177
	v_max_f32_e32 v162, v162, v162
	v_mul_f32_e32 v134, 0xbfb8aa3b, v134
	v_med3_f32 v162, v162, s35, v177
	v_exp_f32_e32 v161, v134
	v_add_f32_e32 v134, 1.0, v185
	v_mul_f32_e32 v162, 0xbfb8aa3b, v162
	v_rcp_f32_e32 v185, v134
	v_max_f32_e32 v134, v186, v186
	v_exp_f32_e32 v186, v162
	v_cvt_pk_f32_fp8_e32 v[182:183], v179
	v_max_f32_e32 v163, v163, v163
	v_med3_f32 v134, v134, s35, v177
	v_med3_f32 v163, v163, s35, v177
	v_mul_f32_e32 v134, 0xbfb8aa3b, v134
	v_mul_f32_e32 v163, 0xbfb8aa3b, v163
	v_pk_add_f32 v[160:161], v[160:161], 1.0 op_sel_hi:[1,0]
	v_exp_f32_e32 v162, v134
	v_add_f32_e32 v134, 1.0, v186
	v_max_f32_e32 v186, v187, v187
	v_exp_f32_e32 v187, v163
	v_pk_mul_f32 v[160:161], v[184:185], v[160:161]
	v_cvt_pk_f32_fp8_e32 v[188:189], v181
	v_pk_mul_f32 v[122:123], v[122:123], v[160:161]
	v_max_f32_e32 v160, v182, v182
	v_med3_f32 v160, v160, s35, v177
	v_med3_f32 v186, v186, s35, v177
	v_mul_f32_e32 v160, 0xbfb8aa3b, v160
	v_mul_f32_e32 v163, 0xbfb8aa3b, v186
	v_rcp_f32_e32 v186, v134
	v_add_f32_e32 v134, 1.0, v187
	v_exp_f32_e32 v161, v160
	v_exp_f32_e32 v163, v163
	v_rcp_f32_e32 v187, v134
	v_max_f32_e32 v134, v188, v188
	v_med3_f32 v134, v134, s35, v177
	v_mul_f32_e32 v134, 0xbfb8aa3b, v134
	v_exp_f32_e32 v160, v134
	v_add_f32_e32 v134, 1.0, v161
	v_max_f32_e32 v161, v183, v183
	v_cvt_pk_f32_fp8_sdwa v[178:179], v179 src0_sel:WORD_1
	v_pk_add_f32 v[162:163], v[162:163], 1.0 op_sel_hi:[1,0]
	v_med3_f32 v161, v161, s35, v177
	v_pk_mul_f32 v[162:163], v[186:187], v[162:163]
	v_mul_f32_e32 v161, 0xbfb8aa3b, v161
	v_pk_mul_f32 v[124:125], v[124:125], v[162:163]
	v_exp_f32_e32 v163, v161
	v_cvt_pk_f32_fp8_sdwa v[180:181], v181 src0_sel:WORD_1
	v_rcp_f32_e32 v162, v134
	v_max_f32_e32 v134, v189, v189
	v_med3_f32 v134, v134, s35, v177
	v_max_f32_e32 v178, v178, v178
	v_mul_f32_e32 v134, 0xbfb8aa3b, v134
	v_med3_f32 v178, v178, s35, v177
	v_exp_f32_e32 v161, v134
	v_add_f32_e32 v134, 1.0, v163
	v_mul_f32_e32 v178, 0xbfb8aa3b, v178
	v_rcp_f32_e32 v163, v134
	v_max_f32_e32 v134, v180, v180
	v_exp_f32_e32 v180, v178
	v_max_f32_e32 v179, v179, v179
	v_med3_f32 v134, v134, s35, v177
	v_med3_f32 v179, v179, s35, v177
	v_mul_f32_e32 v134, 0xbfb8aa3b, v134
	v_mul_f32_e32 v179, 0xbfb8aa3b, v179
	v_exp_f32_e32 v178, v134
	v_add_f32_e32 v134, 1.0, v180
	v_max_f32_e32 v180, v181, v181
	v_exp_f32_e32 v181, v179
	v_med3_f32 v180, v180, s35, v177
	v_mul_f32_e32 v179, 0xbfb8aa3b, v180
	v_exp_f32_e32 v179, v179
	v_rcp_f32_e32 v180, v134
	v_add_f32_e32 v134, 1.0, v181
	v_pk_add_f32 v[160:161], v[160:161], 1.0 op_sel_hi:[1,0]
	v_rcp_f32_e32 v181, v134
	v_pk_mul_f32 v[160:161], v[162:163], v[160:161]
	v_pk_add_f32 v[178:179], v[178:179], 1.0 op_sel_hi:[1,0]
	v_pk_mul_f32 v[110:111], v[110:111], v[160:161]
	s_waitcnt vmcnt(11)
	v_cvt_pk_f32_fp8_e32 v[160:161], v158
	v_pk_mul_f32 v[162:163], v[180:181], v[178:179]
	s_waitcnt vmcnt(10)
	v_cvt_pk_f32_fp8_e32 v[180:181], v156
	v_pk_mul_f32 v[112:113], v[112:113], v[162:163]
	v_max_f32_e32 v160, v160, v160
	v_med3_f32 v160, v160, s35, v177
	v_mul_f32_e32 v160, 0xbfb8aa3b, v160
	v_max_f32_e32 v134, v180, v180
	v_exp_f32_e32 v180, v160
	v_med3_f32 v134, v134, s35, v177
	v_max_f32_e32 v161, v161, v161
	v_cvt_pk_f32_fp8_sdwa v[162:163], v158 src0_sel:WORD_1
	v_mul_f32_e32 v134, 0xbfb8aa3b, v134
	v_med3_f32 v161, v161, s35, v177
	v_exp_f32_e32 v160, v134
	v_add_f32_e32 v134, 1.0, v180
	v_mul_f32_e32 v161, 0xbfb8aa3b, v161
	v_rcp_f32_e32 v180, v134
	v_max_f32_e32 v134, v181, v181
	v_exp_f32_e32 v181, v161
	v_cvt_pk_f32_fp8_sdwa v[182:183], v156 src0_sel:WORD_1
	v_med3_f32 v134, v134, s35, v177
	v_max_f32_e32 v162, v162, v162
	v_mul_f32_e32 v134, 0xbfb8aa3b, v134
	v_med3_f32 v162, v162, s35, v177
	v_exp_f32_e32 v161, v134
	v_add_f32_e32 v134, 1.0, v181
	v_mul_f32_e32 v162, 0xbfb8aa3b, v162
	v_rcp_f32_e32 v181, v134
	v_max_f32_e32 v134, v182, v182
	v_exp_f32_e32 v182, v162
	v_cvt_pk_f32_fp8_e32 v[178:179], v159
	v_max_f32_e32 v163, v163, v163
	v_med3_f32 v134, v134, s35, v177
	v_med3_f32 v163, v163, s35, v177
	v_mul_f32_e32 v134, 0xbfb8aa3b, v134
	v_mul_f32_e32 v163, 0xbfb8aa3b, v163
	v_pk_add_f32 v[160:161], v[160:161], 1.0 op_sel_hi:[1,0]
	v_exp_f32_e32 v162, v134
	v_add_f32_e32 v134, 1.0, v182
	v_max_f32_e32 v182, v183, v183
	v_exp_f32_e32 v183, v163
	v_pk_mul_f32 v[160:161], v[180:181], v[160:161]
	v_cvt_pk_f32_fp8_e32 v[184:185], v157
	v_pk_mul_f32 v[98:99], v[98:99], v[160:161]
	v_max_f32_e32 v160, v178, v178
	v_med3_f32 v160, v160, s35, v177
	v_med3_f32 v182, v182, s35, v177
	v_mul_f32_e32 v160, 0xbfb8aa3b, v160
	v_mul_f32_e32 v163, 0xbfb8aa3b, v182
	v_rcp_f32_e32 v182, v134
	v_add_f32_e32 v134, 1.0, v183
	v_exp_f32_e32 v161, v160
	v_exp_f32_e32 v163, v163
	v_rcp_f32_e32 v183, v134
	v_max_f32_e32 v134, v184, v184
	v_med3_f32 v134, v134, s35, v177
	v_mul_f32_e32 v134, 0xbfb8aa3b, v134
	v_exp_f32_e32 v160, v134
	v_add_f32_e32 v134, 1.0, v161
	v_max_f32_e32 v161, v179, v179
	v_pk_add_f32 v[162:163], v[162:163], 1.0 op_sel_hi:[1,0]
	v_med3_f32 v161, v161, s35, v177
	v_pk_mul_f32 v[162:163], v[182:183], v[162:163]
	v_mul_f32_e32 v161, 0xbfb8aa3b, v161
	v_pk_mul_f32 v[100:101], v[100:101], v[162:163]
	v_exp_f32_e32 v163, v161
	v_cvt_pk_f32_fp8_sdwa v[158:159], v159 src0_sel:WORD_1
	v_cvt_pk_f32_fp8_sdwa v[156:157], v157 src0_sel:WORD_1
	v_rcp_f32_e32 v162, v134
	v_max_f32_e32 v134, v185, v185
	v_med3_f32 v134, v134, s35, v177
	v_mul_f32_e32 v134, 0xbfb8aa3b, v134
	v_exp_f32_e32 v161, v134
	v_add_f32_e32 v134, 1.0, v163
	v_rcp_f32_e32 v163, v134
	v_max_f32_e32 v134, v156, v156
	v_max_f32_e32 v156, v158, v158
	v_med3_f32 v156, v156, s35, v177
	v_mul_f32_e32 v156, 0xbfb8aa3b, v156
	v_exp_f32_e32 v158, v156
	v_med3_f32 v134, v134, s35, v177
	v_mul_f32_e32 v134, 0xbfb8aa3b, v134
	v_exp_f32_e32 v156, v134
	v_add_f32_e32 v134, 1.0, v158
	v_max_f32_e32 v158, v159, v159
	v_med3_f32 v158, v158, s35, v177
	v_mul_f32_e32 v158, 0xbfb8aa3b, v158
	v_exp_f32_e32 v159, v158
	v_max_f32_e32 v157, v157, v157
	v_med3_f32 v157, v157, s35, v177
	v_mul_f32_e32 v157, 0xbfb8aa3b, v157
	v_exp_f32_e32 v157, v157
	v_rcp_f32_e32 v158, v134
	v_add_f32_e32 v134, 1.0, v159
	v_rcp_f32_e32 v159, v134
	v_pk_add_f32 v[156:157], v[156:157], 1.0 op_sel_hi:[1,0]
	v_pk_add_f32 v[160:161], v[160:161], 1.0 op_sel_hi:[1,0]
	s_waitcnt vmcnt(8)
	v_cvt_pk_f32_fp8_sdwa v[178:179], v152 src0_sel:WORD_1
	v_pk_mul_f32 v[156:157], v[158:159], v[156:157]
	v_pk_mul_f32 v[160:161], v[162:163], v[160:161]
	v_pk_mul_f32 v[88:89], v[88:89], v[156:157]
	v_cvt_pk_f32_fp8_e32 v[156:157], v154
	v_cvt_pk_f32_fp8_e32 v[162:163], v152
	v_cvt_pk_f32_fp8_sdwa v[158:159], v154 src0_sel:WORD_1
	v_pk_mul_f32 v[86:87], v[86:87], v[160:161]
	v_max_f32_e32 v156, v156, v156
	v_med3_f32 v156, v156, s35, v177
	v_mul_f32_e32 v156, 0xbfb8aa3b, v156
	v_max_f32_e32 v134, v162, v162
	v_exp_f32_e32 v162, v156
	v_med3_f32 v134, v134, s35, v177
	v_max_f32_e32 v157, v157, v157
	v_mul_f32_e32 v134, 0xbfb8aa3b, v134
	v_med3_f32 v157, v157, s35, v177
	v_exp_f32_e32 v156, v134
	v_add_f32_e32 v134, 1.0, v162
	v_mul_f32_e32 v157, 0xbfb8aa3b, v157
	v_rcp_f32_e32 v162, v134
	v_max_f32_e32 v134, v163, v163
	v_exp_f32_e32 v163, v157
	v_med3_f32 v134, v134, s35, v177
	v_max_f32_e32 v158, v158, v158
	v_mul_f32_e32 v134, 0xbfb8aa3b, v134
	v_med3_f32 v158, v158, s35, v177
	v_exp_f32_e32 v157, v134
	v_add_f32_e32 v134, 1.0, v163
	v_mul_f32_e32 v158, 0xbfb8aa3b, v158
	v_rcp_f32_e32 v163, v134
	v_max_f32_e32 v134, v178, v178
	v_exp_f32_e32 v178, v158
	v_cvt_pk_f32_fp8_e32 v[160:161], v155
	v_max_f32_e32 v159, v159, v159
	v_med3_f32 v134, v134, s35, v177
	v_med3_f32 v159, v159, s35, v177
	v_mul_f32_e32 v134, 0xbfb8aa3b, v134
	v_mul_f32_e32 v159, 0xbfb8aa3b, v159
	v_pk_add_f32 v[156:157], v[156:157], 1.0 op_sel_hi:[1,0]
	v_exp_f32_e32 v158, v134
	v_add_f32_e32 v134, 1.0, v178
	v_max_f32_e32 v178, v179, v179
	v_exp_f32_e32 v179, v159
	v_pk_mul_f32 v[156:157], v[162:163], v[156:157]
	v_cvt_pk_f32_fp8_e32 v[180:181], v153
	v_pk_mul_f32 v[70:71], v[70:71], v[156:157]
	v_max_f32_e32 v156, v160, v160
	v_med3_f32 v156, v156, s35, v177
	v_med3_f32 v178, v178, s35, v177
	v_mul_f32_e32 v156, 0xbfb8aa3b, v156
	v_mul_f32_e32 v159, 0xbfb8aa3b, v178
	v_rcp_f32_e32 v178, v134
	v_add_f32_e32 v134, 1.0, v179
	v_exp_f32_e32 v157, v156
	v_exp_f32_e32 v159, v159
	v_rcp_f32_e32 v179, v134
	v_max_f32_e32 v134, v180, v180
	v_med3_f32 v134, v134, s35, v177
	v_mul_f32_e32 v134, 0xbfb8aa3b, v134
	v_exp_f32_e32 v156, v134
	v_add_f32_e32 v134, 1.0, v157
	v_max_f32_e32 v157, v161, v161
	v_pk_add_f32 v[158:159], v[158:159], 1.0 op_sel_hi:[1,0]
	v_med3_f32 v157, v157, s35, v177
	v_pk_mul_f32 v[158:159], v[178:179], v[158:159]
	v_mul_f32_e32 v157, 0xbfb8aa3b, v157
	v_pk_mul_f32 v[72:73], v[72:73], v[158:159]
	v_exp_f32_e32 v159, v157
	v_cvt_pk_f32_fp8_sdwa v[154:155], v155 src0_sel:WORD_1
	v_cvt_pk_f32_fp8_sdwa v[152:153], v153 src0_sel:WORD_1
	v_rcp_f32_e32 v158, v134
	v_max_f32_e32 v134, v181, v181
	v_med3_f32 v134, v134, s35, v177
	v_mul_f32_e32 v134, 0xbfb8aa3b, v134
	v_exp_f32_e32 v157, v134
	v_add_f32_e32 v134, 1.0, v159
	v_rcp_f32_e32 v159, v134
	v_max_f32_e32 v134, v152, v152
	v_max_f32_e32 v152, v154, v154
	v_med3_f32 v152, v152, s35, v177
	v_mul_f32_e32 v152, 0xbfb8aa3b, v152
	v_exp_f32_e32 v154, v152
	v_med3_f32 v134, v134, s35, v177
	v_mul_f32_e32 v134, 0xbfb8aa3b, v134
	v_exp_f32_e32 v152, v134
	v_add_f32_e32 v134, 1.0, v154
	v_max_f32_e32 v154, v155, v155
	v_med3_f32 v154, v154, s35, v177
	v_mul_f32_e32 v154, 0xbfb8aa3b, v154
	v_exp_f32_e32 v155, v154
	v_max_f32_e32 v153, v153, v153
	v_med3_f32 v153, v153, s35, v177
	v_mul_f32_e32 v153, 0xbfb8aa3b, v153
	v_exp_f32_e32 v153, v153
	v_rcp_f32_e32 v154, v134
	v_add_f32_e32 v134, 1.0, v155
	v_rcp_f32_e32 v155, v134
	v_pk_add_f32 v[152:153], v[152:153], 1.0 op_sel_hi:[1,0]
	v_pk_add_f32 v[156:157], v[156:157], 1.0 op_sel_hi:[1,0]
	s_waitcnt vmcnt(6)
	v_cvt_pk_f32_fp8_sdwa v[160:161], v148 src0_sel:WORD_1
	v_pk_mul_f32 v[152:153], v[154:155], v[152:153]
	v_pk_mul_f32 v[156:157], v[158:159], v[156:157]
	v_pk_mul_f32 v[60:61], v[60:61], v[152:153]
	v_cvt_pk_f32_fp8_e32 v[152:153], v150
	v_cvt_pk_f32_fp8_e32 v[158:159], v148
	v_cvt_pk_f32_fp8_sdwa v[154:155], v150 src0_sel:WORD_1
	v_pk_mul_f32 v[58:59], v[58:59], v[156:157]
	v_max_f32_e32 v152, v152, v152
	v_med3_f32 v152, v152, s35, v177
	v_mul_f32_e32 v152, 0xbfb8aa3b, v152
	v_max_f32_e32 v134, v158, v158
	v_exp_f32_e32 v158, v152
	v_med3_f32 v134, v134, s35, v177
	v_max_f32_e32 v153, v153, v153
	v_mul_f32_e32 v134, 0xbfb8aa3b, v134
	v_med3_f32 v153, v153, s35, v177
	v_exp_f32_e32 v152, v134
	v_add_f32_e32 v134, 1.0, v158
	v_mul_f32_e32 v153, 0xbfb8aa3b, v153
	v_rcp_f32_e32 v158, v134
	v_max_f32_e32 v134, v159, v159
	v_exp_f32_e32 v159, v153
	v_med3_f32 v134, v134, s35, v177
	v_max_f32_e32 v154, v154, v154
	v_mul_f32_e32 v134, 0xbfb8aa3b, v134
	v_med3_f32 v154, v154, s35, v177
	v_exp_f32_e32 v153, v134
	v_add_f32_e32 v134, 1.0, v159
	v_mul_f32_e32 v154, 0xbfb8aa3b, v154
	v_rcp_f32_e32 v159, v134
	v_max_f32_e32 v134, v160, v160
	v_exp_f32_e32 v160, v154
	v_cvt_pk_f32_fp8_e32 v[156:157], v151
	v_max_f32_e32 v155, v155, v155
	v_med3_f32 v134, v134, s35, v177
	v_med3_f32 v155, v155, s35, v177
	v_mul_f32_e32 v134, 0xbfb8aa3b, v134
	v_mul_f32_e32 v155, 0xbfb8aa3b, v155
	v_pk_add_f32 v[152:153], v[152:153], 1.0 op_sel_hi:[1,0]
	v_exp_f32_e32 v154, v134
	v_add_f32_e32 v134, 1.0, v160
	v_max_f32_e32 v160, v161, v161
	v_exp_f32_e32 v161, v155
	v_pk_mul_f32 v[152:153], v[158:159], v[152:153]
	v_cvt_pk_f32_fp8_e32 v[162:163], v149
	v_pk_mul_f32 v[46:47], v[46:47], v[152:153]
	v_max_f32_e32 v152, v156, v156
	v_med3_f32 v152, v152, s35, v177
	v_med3_f32 v160, v160, s35, v177
	v_mul_f32_e32 v152, 0xbfb8aa3b, v152
	v_mul_f32_e32 v155, 0xbfb8aa3b, v160
	v_rcp_f32_e32 v160, v134
	v_add_f32_e32 v134, 1.0, v161
	v_exp_f32_e32 v153, v152
	v_exp_f32_e32 v155, v155
	v_rcp_f32_e32 v161, v134
	v_max_f32_e32 v134, v162, v162
	v_med3_f32 v134, v134, s35, v177
	v_mul_f32_e32 v134, 0xbfb8aa3b, v134
	v_exp_f32_e32 v152, v134
	v_add_f32_e32 v134, 1.0, v153
	v_max_f32_e32 v153, v157, v157
	v_pk_add_f32 v[154:155], v[154:155], 1.0 op_sel_hi:[1,0]
	v_med3_f32 v153, v153, s35, v177
	v_pk_mul_f32 v[154:155], v[160:161], v[154:155]
	v_mul_f32_e32 v153, 0xbfb8aa3b, v153
	v_pk_mul_f32 v[48:49], v[48:49], v[154:155]
	v_exp_f32_e32 v155, v153
	v_cvt_pk_f32_fp8_sdwa v[150:151], v151 src0_sel:WORD_1
	v_cvt_pk_f32_fp8_sdwa v[148:149], v149 src0_sel:WORD_1
	v_rcp_f32_e32 v154, v134
	v_max_f32_e32 v134, v163, v163
	v_med3_f32 v134, v134, s35, v177
	v_mul_f32_e32 v134, 0xbfb8aa3b, v134
	v_exp_f32_e32 v153, v134
	v_add_f32_e32 v134, 1.0, v155
	v_rcp_f32_e32 v155, v134
	v_max_f32_e32 v134, v148, v148
	v_max_f32_e32 v148, v150, v150
	v_med3_f32 v148, v148, s35, v177
	v_mul_f32_e32 v148, 0xbfb8aa3b, v148
	v_exp_f32_e32 v150, v148
	v_med3_f32 v134, v134, s35, v177
	v_mul_f32_e32 v134, 0xbfb8aa3b, v134
	v_exp_f32_e32 v148, v134
	v_add_f32_e32 v134, 1.0, v150
	v_max_f32_e32 v150, v151, v151
	v_med3_f32 v150, v150, s35, v177
	v_mul_f32_e32 v150, 0xbfb8aa3b, v150
	v_exp_f32_e32 v151, v150
	v_max_f32_e32 v149, v149, v149
	v_med3_f32 v149, v149, s35, v177
	v_mul_f32_e32 v149, 0xbfb8aa3b, v149
	v_exp_f32_e32 v149, v149
	v_rcp_f32_e32 v150, v134
	v_add_f32_e32 v134, 1.0, v151
	v_rcp_f32_e32 v151, v134
	v_pk_add_f32 v[148:149], v[148:149], 1.0 op_sel_hi:[1,0]
	v_pk_add_f32 v[152:153], v[152:153], 1.0 op_sel_hi:[1,0]
	s_waitcnt vmcnt(4)
	v_cvt_pk_f32_fp8_sdwa v[156:157], v144 src0_sel:WORD_1
	v_pk_mul_f32 v[148:149], v[150:151], v[148:149]
	v_pk_mul_f32 v[152:153], v[154:155], v[152:153]
	v_pk_mul_f32 v[36:37], v[36:37], v[148:149]
	v_cvt_pk_f32_fp8_e32 v[148:149], v146
	v_cvt_pk_f32_fp8_e32 v[154:155], v144
	v_cvt_pk_f32_fp8_sdwa v[150:151], v146 src0_sel:WORD_1
	v_pk_mul_f32 v[34:35], v[34:35], v[152:153]
	v_max_f32_e32 v148, v148, v148
	v_med3_f32 v148, v148, s35, v177
	v_mul_f32_e32 v148, 0xbfb8aa3b, v148
	v_max_f32_e32 v134, v154, v154
	v_exp_f32_e32 v154, v148
	v_med3_f32 v134, v134, s35, v177
	v_max_f32_e32 v149, v149, v149
	v_mul_f32_e32 v134, 0xbfb8aa3b, v134
	v_med3_f32 v149, v149, s35, v177
	v_exp_f32_e32 v148, v134
	v_add_f32_e32 v134, 1.0, v154
	v_mul_f32_e32 v149, 0xbfb8aa3b, v149
	v_rcp_f32_e32 v154, v134
	v_max_f32_e32 v134, v155, v155
	v_exp_f32_e32 v155, v149
	v_med3_f32 v134, v134, s35, v177
	v_max_f32_e32 v150, v150, v150
	v_mul_f32_e32 v134, 0xbfb8aa3b, v134
	v_med3_f32 v150, v150, s35, v177
	v_exp_f32_e32 v149, v134
	v_add_f32_e32 v134, 1.0, v155
	v_mul_f32_e32 v150, 0xbfb8aa3b, v150
	v_rcp_f32_e32 v155, v134
	v_max_f32_e32 v134, v156, v156
	v_exp_f32_e32 v156, v150
	v_cvt_pk_f32_fp8_e32 v[152:153], v147
	v_max_f32_e32 v151, v151, v151
	v_med3_f32 v134, v134, s35, v177
	v_med3_f32 v151, v151, s35, v177
	v_mul_f32_e32 v134, 0xbfb8aa3b, v134
	v_mul_f32_e32 v151, 0xbfb8aa3b, v151
	v_pk_add_f32 v[148:149], v[148:149], 1.0 op_sel_hi:[1,0]
	v_exp_f32_e32 v150, v134
	v_add_f32_e32 v134, 1.0, v156
	v_max_f32_e32 v156, v157, v157
	v_exp_f32_e32 v157, v151
	v_pk_mul_f32 v[148:149], v[154:155], v[148:149]
	v_cvt_pk_f32_fp8_e32 v[158:159], v145
	v_pk_mul_f32 v[22:23], v[22:23], v[148:149]
	v_max_f32_e32 v148, v152, v152
	v_med3_f32 v148, v148, s35, v177
	v_med3_f32 v156, v156, s35, v177
	v_mul_f32_e32 v148, 0xbfb8aa3b, v148
	v_mul_f32_e32 v151, 0xbfb8aa3b, v156
	v_rcp_f32_e32 v156, v134
	v_add_f32_e32 v134, 1.0, v157
	v_exp_f32_e32 v149, v148
	v_exp_f32_e32 v151, v151
	v_rcp_f32_e32 v157, v134
	v_max_f32_e32 v134, v158, v158
	v_med3_f32 v134, v134, s35, v177
	v_mul_f32_e32 v134, 0xbfb8aa3b, v134
	v_exp_f32_e32 v148, v134
	v_add_f32_e32 v134, 1.0, v149
	v_max_f32_e32 v149, v153, v153
	v_pk_add_f32 v[150:151], v[150:151], 1.0 op_sel_hi:[1,0]
	v_med3_f32 v149, v149, s35, v177
	v_pk_mul_f32 v[150:151], v[156:157], v[150:151]
	v_mul_f32_e32 v149, 0xbfb8aa3b, v149
	v_pk_mul_f32 v[24:25], v[24:25], v[150:151]
	v_exp_f32_e32 v151, v149
	v_cvt_pk_f32_fp8_sdwa v[146:147], v147 src0_sel:WORD_1
	v_cvt_pk_f32_fp8_sdwa v[144:145], v145 src0_sel:WORD_1
	v_rcp_f32_e32 v150, v134
	v_max_f32_e32 v134, v159, v159
	v_med3_f32 v134, v134, s35, v177
	v_mul_f32_e32 v134, 0xbfb8aa3b, v134
	v_exp_f32_e32 v149, v134
	v_add_f32_e32 v134, 1.0, v151
	v_rcp_f32_e32 v151, v134
	v_max_f32_e32 v134, v144, v144
	v_max_f32_e32 v144, v146, v146
	v_med3_f32 v144, v144, s35, v177
	v_mul_f32_e32 v144, 0xbfb8aa3b, v144
	v_exp_f32_e32 v146, v144
	v_med3_f32 v134, v134, s35, v177
	v_mul_f32_e32 v134, 0xbfb8aa3b, v134
	v_exp_f32_e32 v144, v134
	v_add_f32_e32 v134, 1.0, v146
	v_max_f32_e32 v146, v147, v147
	v_med3_f32 v146, v146, s35, v177
	v_mul_f32_e32 v146, 0xbfb8aa3b, v146
	v_exp_f32_e32 v147, v146
	v_max_f32_e32 v145, v145, v145
	v_med3_f32 v145, v145, s35, v177
	v_mul_f32_e32 v145, 0xbfb8aa3b, v145
	v_exp_f32_e32 v145, v145
	v_rcp_f32_e32 v146, v134
	v_add_f32_e32 v134, 1.0, v147
	v_rcp_f32_e32 v147, v134
	v_pk_add_f32 v[144:145], v[144:145], 1.0 op_sel_hi:[1,0]
	v_pk_add_f32 v[148:149], v[148:149], 1.0 op_sel_hi:[1,0]
	s_waitcnt vmcnt(2)
	v_cvt_pk_f32_fp8_sdwa v[152:153], v140 src0_sel:WORD_1
	v_pk_mul_f32 v[144:145], v[146:147], v[144:145]
	v_pk_mul_f32 v[148:149], v[150:151], v[148:149]
	v_pk_mul_f32 v[20:21], v[20:21], v[144:145]
	v_cvt_pk_f32_fp8_e32 v[144:145], v142
	v_cvt_pk_f32_fp8_e32 v[150:151], v140
	v_cvt_pk_f32_fp8_sdwa v[146:147], v142 src0_sel:WORD_1
	v_pk_mul_f32 v[18:19], v[18:19], v[148:149]
	v_max_f32_e32 v144, v144, v144
	v_med3_f32 v144, v144, s35, v177
	v_mul_f32_e32 v144, 0xbfb8aa3b, v144
	v_max_f32_e32 v134, v150, v150
	v_exp_f32_e32 v150, v144
	v_med3_f32 v134, v134, s35, v177
	v_max_f32_e32 v145, v145, v145
	v_mul_f32_e32 v134, 0xbfb8aa3b, v134
	v_med3_f32 v145, v145, s35, v177
	v_exp_f32_e32 v144, v134
	v_add_f32_e32 v134, 1.0, v150
	v_mul_f32_e32 v145, 0xbfb8aa3b, v145
	v_rcp_f32_e32 v150, v134
	v_max_f32_e32 v134, v151, v151
	v_exp_f32_e32 v151, v145
	v_med3_f32 v134, v134, s35, v177
	v_max_f32_e32 v146, v146, v146
	v_mul_f32_e32 v134, 0xbfb8aa3b, v134
	v_med3_f32 v146, v146, s35, v177
	v_exp_f32_e32 v145, v134
	v_add_f32_e32 v134, 1.0, v151
	v_mul_f32_e32 v146, 0xbfb8aa3b, v146
	v_rcp_f32_e32 v151, v134
	v_max_f32_e32 v134, v152, v152
	v_exp_f32_e32 v152, v146
	v_cvt_pk_f32_fp8_e32 v[148:149], v143
	v_max_f32_e32 v147, v147, v147
	v_med3_f32 v134, v134, s35, v177
	v_med3_f32 v147, v147, s35, v177
	v_mul_f32_e32 v134, 0xbfb8aa3b, v134
	v_mul_f32_e32 v147, 0xbfb8aa3b, v147
	v_pk_add_f32 v[144:145], v[144:145], 1.0 op_sel_hi:[1,0]
	v_exp_f32_e32 v146, v134
	v_add_f32_e32 v134, 1.0, v152
	v_max_f32_e32 v152, v153, v153
	v_exp_f32_e32 v153, v147
	v_pk_mul_f32 v[144:145], v[150:151], v[144:145]
	v_cvt_pk_f32_fp8_e32 v[154:155], v141
	v_pk_mul_f32 v[14:15], v[14:15], v[144:145]
	v_max_f32_e32 v144, v148, v148
	v_med3_f32 v144, v144, s35, v177
	v_med3_f32 v152, v152, s35, v177
	v_mul_f32_e32 v144, 0xbfb8aa3b, v144
	v_mul_f32_e32 v147, 0xbfb8aa3b, v152
	v_rcp_f32_e32 v152, v134
	v_add_f32_e32 v134, 1.0, v153
	v_exp_f32_e32 v145, v144
	v_exp_f32_e32 v147, v147
	v_rcp_f32_e32 v153, v134
	v_max_f32_e32 v134, v154, v154
	v_med3_f32 v134, v134, s35, v177
	v_mul_f32_e32 v134, 0xbfb8aa3b, v134
	v_exp_f32_e32 v144, v134
	v_add_f32_e32 v134, 1.0, v145
	v_max_f32_e32 v145, v149, v149
	v_pk_add_f32 v[146:147], v[146:147], 1.0 op_sel_hi:[1,0]
	v_med3_f32 v145, v145, s35, v177
	v_pk_mul_f32 v[146:147], v[152:153], v[146:147]
	v_mul_f32_e32 v145, 0xbfb8aa3b, v145
	v_pk_mul_f32 v[16:17], v[16:17], v[146:147]
	v_exp_f32_e32 v147, v145
	v_cvt_pk_f32_fp8_sdwa v[142:143], v143 src0_sel:WORD_1
	v_cvt_pk_f32_fp8_sdwa v[140:141], v141 src0_sel:WORD_1
	v_rcp_f32_e32 v146, v134
	v_max_f32_e32 v134, v155, v155
	v_med3_f32 v134, v134, s35, v177
	v_mul_f32_e32 v134, 0xbfb8aa3b, v134
	v_exp_f32_e32 v145, v134
	v_add_f32_e32 v134, 1.0, v147
	v_rcp_f32_e32 v147, v134
	v_max_f32_e32 v134, v140, v140
	v_max_f32_e32 v140, v142, v142
	v_med3_f32 v140, v140, s35, v177
	v_mul_f32_e32 v140, 0xbfb8aa3b, v140
	v_exp_f32_e32 v142, v140
	v_med3_f32 v134, v134, s35, v177
	v_mul_f32_e32 v134, 0xbfb8aa3b, v134
	v_exp_f32_e32 v140, v134
	v_add_f32_e32 v134, 1.0, v142
	v_max_f32_e32 v142, v143, v143
	v_med3_f32 v142, v142, s35, v177
	v_mul_f32_e32 v142, 0xbfb8aa3b, v142
	v_exp_f32_e32 v143, v142
	v_max_f32_e32 v141, v141, v141
	v_med3_f32 v141, v141, s35, v177
	v_mul_f32_e32 v141, 0xbfb8aa3b, v141
	v_exp_f32_e32 v141, v141
	v_rcp_f32_e32 v142, v134
	v_add_f32_e32 v134, 1.0, v143
	v_rcp_f32_e32 v143, v134
	v_pk_add_f32 v[140:141], v[140:141], 1.0 op_sel_hi:[1,0]
	v_pk_add_f32 v[144:145], v[144:145], 1.0 op_sel_hi:[1,0]
	s_waitcnt vmcnt(0)
	v_cvt_pk_f32_fp8_sdwa v[148:149], v136 src0_sel:WORD_1
	v_pk_mul_f32 v[140:141], v[142:143], v[140:141]
	v_pk_mul_f32 v[144:145], v[146:147], v[144:145]
	v_pk_mul_f32 v[12:13], v[12:13], v[140:141]
	v_cvt_pk_f32_fp8_e32 v[140:141], v138
	v_cvt_pk_f32_fp8_e32 v[146:147], v136
	v_cvt_pk_f32_fp8_sdwa v[142:143], v138 src0_sel:WORD_1
	v_pk_mul_f32 v[10:11], v[10:11], v[144:145]
	v_max_f32_e32 v140, v140, v140
	v_med3_f32 v140, v140, s35, v177
	v_mul_f32_e32 v140, 0xbfb8aa3b, v140
	v_max_f32_e32 v134, v146, v146
	v_exp_f32_e32 v146, v140
	v_med3_f32 v134, v134, s35, v177
	v_max_f32_e32 v141, v141, v141
	v_mul_f32_e32 v134, 0xbfb8aa3b, v134
	v_med3_f32 v141, v141, s35, v177
	v_exp_f32_e32 v140, v134
	v_add_f32_e32 v134, 1.0, v146
	v_mul_f32_e32 v141, 0xbfb8aa3b, v141
	v_rcp_f32_e32 v146, v134
	v_max_f32_e32 v134, v147, v147
	v_exp_f32_e32 v147, v141
	v_med3_f32 v134, v134, s35, v177
	v_max_f32_e32 v142, v142, v142
	v_mul_f32_e32 v134, 0xbfb8aa3b, v134
	v_med3_f32 v142, v142, s35, v177
	v_exp_f32_e32 v141, v134
	v_add_f32_e32 v134, 1.0, v147
	v_mul_f32_e32 v142, 0xbfb8aa3b, v142
	v_rcp_f32_e32 v147, v134
	v_max_f32_e32 v134, v148, v148
	v_exp_f32_e32 v148, v142
	v_cvt_pk_f32_fp8_e32 v[144:145], v139
	v_max_f32_e32 v143, v143, v143
	v_med3_f32 v134, v134, s35, v177
	v_med3_f32 v143, v143, s35, v177
	v_mul_f32_e32 v134, 0xbfb8aa3b, v134
	v_mul_f32_e32 v143, 0xbfb8aa3b, v143
	v_pk_add_f32 v[140:141], v[140:141], 1.0 op_sel_hi:[1,0]
	v_exp_f32_e32 v142, v134
	v_add_f32_e32 v134, 1.0, v148
	v_max_f32_e32 v148, v149, v149
	v_exp_f32_e32 v149, v143
	v_pk_mul_f32 v[140:141], v[146:147], v[140:141]
	v_cvt_pk_f32_fp8_e32 v[150:151], v137
	v_pk_mul_f32 v[6:7], v[6:7], v[140:141]
	v_max_f32_e32 v140, v144, v144
	v_med3_f32 v140, v140, s35, v177
	v_med3_f32 v148, v148, s35, v177
	v_mul_f32_e32 v140, 0xbfb8aa3b, v140
	v_mul_f32_e32 v143, 0xbfb8aa3b, v148
	v_rcp_f32_e32 v148, v134
	v_add_f32_e32 v134, 1.0, v149
	v_exp_f32_e32 v141, v140
	v_exp_f32_e32 v143, v143
	v_rcp_f32_e32 v149, v134
	v_max_f32_e32 v134, v150, v150
	v_med3_f32 v134, v134, s35, v177
	v_mul_f32_e32 v134, 0xbfb8aa3b, v134
	v_exp_f32_e32 v140, v134
	v_add_f32_e32 v134, 1.0, v141
	v_max_f32_e32 v141, v145, v145
	v_pk_add_f32 v[142:143], v[142:143], 1.0 op_sel_hi:[1,0]
	v_med3_f32 v141, v141, s35, v177
	v_pk_mul_f32 v[142:143], v[148:149], v[142:143]
	v_mul_f32_e32 v141, 0xbfb8aa3b, v141
	v_pk_mul_f32 v[8:9], v[8:9], v[142:143]
	v_exp_f32_e32 v143, v141
	v_cvt_pk_f32_fp8_sdwa v[138:139], v139 src0_sel:WORD_1
	v_cvt_pk_f32_fp8_sdwa v[136:137], v137 src0_sel:WORD_1
	v_rcp_f32_e32 v142, v134
	v_max_f32_e32 v134, v151, v151
	v_med3_f32 v134, v134, s35, v177
	v_mul_f32_e32 v134, 0xbfb8aa3b, v134
	v_exp_f32_e32 v141, v134
	v_add_f32_e32 v134, 1.0, v143
	v_rcp_f32_e32 v143, v134
	v_max_f32_e32 v134, v136, v136
	v_max_f32_e32 v136, v138, v138
	v_med3_f32 v136, v136, s35, v177
	v_mul_f32_e32 v136, 0xbfb8aa3b, v136
	v_exp_f32_e32 v138, v136
	v_med3_f32 v134, v134, s35, v177
	v_mul_f32_e32 v134, 0xbfb8aa3b, v134
	v_exp_f32_e32 v136, v134
	v_add_f32_e32 v134, 1.0, v138
	v_max_f32_e32 v138, v139, v139
	v_med3_f32 v138, v138, s35, v177
	v_mul_f32_e32 v138, 0xbfb8aa3b, v138
	v_exp_f32_e32 v139, v138
	v_max_f32_e32 v137, v137, v137
	v_med3_f32 v137, v137, s35, v177
	v_mul_f32_e32 v137, 0xbfb8aa3b, v137
	v_exp_f32_e32 v137, v137
	v_rcp_f32_e32 v138, v134
	v_add_f32_e32 v134, 1.0, v139
	v_rcp_f32_e32 v139, v134
	v_pk_add_f32 v[136:137], v[136:137], 1.0 op_sel_hi:[1,0]
	v_pk_add_f32 v[140:141], v[140:141], 1.0 op_sel_hi:[1,0]
	v_pk_mul_f32 v[136:137], v[138:139], v[136:137]
	v_pk_mul_f32 v[140:141], v[142:143], v[140:141]
	v_pk_mul_f32 v[4:5], v[4:5], v[136:137]
	v_pk_mul_f32 v[2:3], v[2:3], v[140:141]
	s_nop 0

.LBB0_1439:
	s_ashr_i32 s21, s20, 31
	s_lshl_b64 s[22:23], s[20:21], 19
	s_add_u32 s22, s89, s22
	s_addc_u32 s23, s24, s23
	s_and_b64 s[54:55], s[40:41], exec
	s_cselect_b32 s21, s23, s59
	s_cselect_b32 s33, s22, s58
	s_ashr_i32 s19, s18, 31
	s_lshl_b64 s[54:55], s[18:19], 19
	s_add_u32 s54, s25, s54
	s_addc_u32 s55, s26, s55
	s_and_b64 s[62:63], s[40:41], exec
	s_cselect_b32 s19, s55, s61
	s_cselect_b32 s84, s54, s60
	s_add_u32 s85, s60, 0x100
	s_addc_u32 s86, s61, 0
	s_mov_b32 s87, -2
	s_waitcnt vmcnt(12)
	s_waitcnt vmcnt(11)
	s_waitcnt vmcnt(8)
	s_waitcnt vmcnt(7)
	s_waitcnt vmcnt(4)
	s_waitcnt vmcnt(3)
	s_waitcnt vmcnt(2)
	s_waitcnt vmcnt(0)
.Lpeel1440:
	ds_read_b128 v[130:133], v234
	ds_read_b128 v[134:137], v234 offset:1024
	ds_read_b128 v[138:141], v234 offset:2048
	ds_read_b128 v[142:145], v234 offset:3072
	ds_read_b128 v[146:149], v235
	ds_read_b128 v[150:153], v235 offset:1024
	ds_read_b128 v[154:157], v235 offset:2048
	ds_read_b128 v[158:161], v235 offset:3072
	s_add_u32 s60, s58, 0x100
	s_addc_u32 s61, s59, 0
	s_cmp_eq_u32 s87, 12
	s_cselect_b32 s66, s33, s60
	s_cselect_b32 s67, s21, s61
	s_cselect_b32 s64, s84, s85
	s_cselect_b32 s65, s19, s86
	s_add_u32 s62, s66, 0x80
	s_addc_u32 s63, s67, 0
	ds_read_b128 v[162:165], v236
	ds_read_b128 v[166:169], v236 offset:1024
	ds_read_b128 v[170:173], v236 offset:2048
	ds_read_b128 v[174:177], v236 offset:3072
	ds_read_b128 v[178:181], v236 offset:4096
	ds_read_b128 v[182:185], v236 offset:5120
	ds_read_b128 v[186:189], v236 offset:6144
	ds_read_b128 v[190:193], v236 offset:7168
	s_add_u32 s58, s58, 0x40080
	s_addc_u32 s59, s59, 0
	s_mov_b32 s88, m0
	s_mov_b32 m0, s80
	s_nop 2
	global_load_lds_dwordx4 v228, s[58:59]
	s_mov_b32 m0, s88
	s_nop 0
	s_mov_b32 s88, m0
	s_mov_b32 m0, s81
	s_nop 2
	global_load_lds_dwordx4 v230, s[58:59]
	s_mov_b32 m0, s88
	s_waitcnt vmcnt(8)
	s_waitcnt lgkmcnt(0)
	s_barrier
	s_setprio 1
	s_waitcnt lgkmcnt(7)
	v_mfma_f32_16x16x32_bf16 v[126:129], v[130:133], v[162:165], 0
	v_mfma_f32_16x16x32_bf16 v[122:125], v[138:141], v[162:165], 0
	s_waitcnt lgkmcnt(5)
	v_mfma_f32_16x16x32_bf16 v[114:117], v[130:133], v[170:173], 0
	v_mfma_f32_16x16x32_bf16 v[106:109], v[138:141], v[170:173], 0
	s_waitcnt lgkmcnt(3)
	v_mfma_f32_16x16x32_bf16 v[94:97], v[130:133], v[178:181], 0
	v_mfma_f32_16x16x32_bf16 v[90:93], v[138:141], v[178:181], 0
	s_waitcnt lgkmcnt(1)
	v_mfma_f32_16x16x32_bf16 v[86:89], v[130:133], v[186:189], 0
	v_mfma_f32_16x16x32_bf16 v[78:81], v[138:141], v[186:189], 0
	v_mfma_f32_16x16x32_bf16 v[126:129], v[134:137], v[166:169], v[126:129]
	v_mfma_f32_16x16x32_bf16 v[122:125], v[142:145], v[166:169], v[122:125]
	v_mfma_f32_16x16x32_bf16 v[114:117], v[134:137], v[174:177], v[114:117]
	v_mfma_f32_16x16x32_bf16 v[106:109], v[142:145], v[174:177], v[106:109]
	v_mfma_f32_16x16x32_bf16 v[94:97], v[134:137], v[182:185], v[94:97]
	v_mfma_f32_16x16x32_bf16 v[90:93], v[142:145], v[182:185], v[90:93]
	s_waitcnt lgkmcnt(0)
	v_mfma_f32_16x16x32_bf16 v[86:89], v[134:137], v[190:193], v[86:89]
	v_mfma_f32_16x16x32_bf16 v[78:81], v[142:145], v[190:193], v[78:81]
	s_setprio 0
	s_setprio 1
	v_mfma_f32_16x16x32_bf16 v[118:121], v[146:149], v[162:165], 0
	v_mfma_f32_16x16x32_bf16 v[110:113], v[154:157], v[162:165], 0
	v_mfma_f32_16x16x32_bf16 v[102:105], v[146:149], v[170:173], 0
	v_mfma_f32_16x16x32_bf16 v[98:101], v[154:157], v[170:173], 0
	v_mfma_f32_16x16x32_bf16 v[82:85], v[146:149], v[178:181], 0
	v_mfma_f32_16x16x32_bf16 v[74:77], v[154:157], v[178:181], 0
	v_mfma_f32_16x16x32_bf16 v[70:73], v[146:149], v[186:189], 0
	v_mfma_f32_16x16x32_bf16 v[66:69], v[154:157], v[186:189], 0
	v_mfma_f32_16x16x32_bf16 v[118:121], v[150:153], v[166:169], v[118:121]
	v_mfma_f32_16x16x32_bf16 v[110:113], v[158:161], v[166:169], v[110:113]
	v_mfma_f32_16x16x32_bf16 v[102:105], v[150:153], v[174:177], v[102:105]
	v_mfma_f32_16x16x32_bf16 v[98:101], v[158:161], v[174:177], v[98:101]
	v_mfma_f32_16x16x32_bf16 v[82:85], v[150:153], v[182:185], v[82:85]
	v_mfma_f32_16x16x32_bf16 v[74:77], v[158:161], v[182:185], v[74:77]
	v_mfma_f32_16x16x32_bf16 v[70:73], v[150:153], v[190:193], v[70:73]
	v_mfma_f32_16x16x32_bf16 v[66:69], v[158:161], v[190:193], v[66:69]
	s_setprio 0
	s_barrier
	ds_read_b128 v[162:165], v236 offset:16384
	ds_read_b128 v[166:169], v236 offset:17408
	ds_read_b128 v[170:173], v236 offset:18432
	ds_read_b128 v[174:177], v236 offset:19456
	ds_read_b128 v[178:181], v236 offset:20480
	ds_read_b128 v[182:185], v236 offset:21504
	ds_read_b128 v[186:189], v236 offset:22528
	ds_read_b128 v[190:193], v236 offset:23552
	s_mov_b32 s58, m0
	s_mov_b32 m0, s30
	s_nop 2
	global_load_lds_dwordx4 v229, s[64:65]
	s_mov_b32 m0, s58
	s_nop 0
	s_mov_b32 s58, m0
	s_mov_b32 m0, s31
	s_nop 2
	global_load_lds_dwordx4 v231, s[64:65]
	s_mov_b32 m0, s58
	s_add_u32 s58, s64, 0x40000
	s_addc_u32 s59, s65, 0
	s_mov_b32 s88, m0
	s_mov_b32 m0, s34
	s_nop 2
	global_load_lds_dwordx4 v229, s[58:59]
	s_mov_b32 m0, s88
	s_nop 0
	s_mov_b32 s88, m0
	s_mov_b32 m0, s35
	s_nop 2
	global_load_lds_dwordx4 v231, s[58:59]
	s_mov_b32 m0, s88
	s_mov_b32 s58, m0
	s_mov_b32 m0, s28
	s_nop 2
	global_load_lds_dwordx4 v228, s[66:67]
	s_mov_b32 m0, s58
	s_nop 0
	s_mov_b32 s58, m0
	s_mov_b32 m0, s36
	s_nop 2
	global_load_lds_dwordx4 v230, s[66:67]
	s_mov_b32 m0, s58
	s_waitcnt vmcnt(8)
	s_waitcnt lgkmcnt(0)
	s_barrier
	s_setprio 1
	s_waitcnt lgkmcnt(7)
	v_mfma_f32_16x16x32_bf16 v[62:65], v[130:133], v[162:165], 0
	v_mfma_f32_16x16x32_bf16 v[58:61], v[138:141], v[162:165], 0
	s_waitcnt lgkmcnt(5)
	v_mfma_f32_16x16x32_bf16 v[54:57], v[130:133], v[170:173], 0
	v_mfma_f32_16x16x32_bf16 v[46:49], v[138:141], v[170:173], 0
	s_waitcnt lgkmcnt(3)
	v_mfma_f32_16x16x32_bf16 v[38:41], v[130:133], v[178:181], 0
	v_mfma_f32_16x16x32_bf16 v[30:33], v[138:141], v[178:181], 0
	s_waitcnt lgkmcnt(1)
	v_mfma_f32_16x16x32_bf16 v[22:25], v[130:133], v[186:189], 0
	v_mfma_f32_16x16x32_bf16 v[14:17], v[138:141], v[186:189], 0
	v_mfma_f32_16x16x32_bf16 v[62:65], v[134:137], v[166:169], v[62:65]
	v_mfma_f32_16x16x32_bf16 v[58:61], v[142:145], v[166:169], v[58:61]
	v_mfma_f32_16x16x32_bf16 v[54:57], v[134:137], v[174:177], v[54:57]
	v_mfma_f32_16x16x32_bf16 v[46:49], v[142:145], v[174:177], v[46:49]
	v_mfma_f32_16x16x32_bf16 v[38:41], v[134:137], v[182:185], v[38:41]
	v_mfma_f32_16x16x32_bf16 v[30:33], v[142:145], v[182:185], v[30:33]
	s_waitcnt lgkmcnt(0)
	v_mfma_f32_16x16x32_bf16 v[22:25], v[134:137], v[190:193], v[22:25]
	v_mfma_f32_16x16x32_bf16 v[14:17], v[142:145], v[190:193], v[14:17]
	s_setprio 0
	s_setprio 1
	v_mfma_f32_16x16x32_bf16 v[50:53], v[146:149], v[162:165], 0
	v_mfma_f32_16x16x32_bf16 v[42:45], v[154:157], v[162:165], 0
	v_mfma_f32_16x16x32_bf16 v[34:37], v[146:149], v[170:173], 0
	v_mfma_f32_16x16x32_bf16 v[26:29], v[154:157], v[170:173], 0
	v_mfma_f32_16x16x32_bf16 v[18:21], v[146:149], v[178:181], 0
	v_mfma_f32_16x16x32_bf16 v[10:13], v[154:157], v[178:181], 0
	v_mfma_f32_16x16x32_bf16 v[6:9], v[146:149], v[186:189], 0
	v_mfma_f32_16x16x32_bf16 v[2:5], v[154:157], v[186:189], 0
	v_mfma_f32_16x16x32_bf16 v[50:53], v[150:153], v[166:169], v[50:53]
	v_mfma_f32_16x16x32_bf16 v[42:45], v[158:161], v[166:169], v[42:45]
	v_mfma_f32_16x16x32_bf16 v[34:37], v[150:153], v[174:177], v[34:37]
	v_mfma_f32_16x16x32_bf16 v[26:29], v[158:161], v[174:177], v[26:29]
	v_mfma_f32_16x16x32_bf16 v[18:21], v[150:153], v[182:185], v[18:21]
	v_mfma_f32_16x16x32_bf16 v[10:13], v[158:161], v[182:185], v[10:13]
	v_mfma_f32_16x16x32_bf16 v[6:9], v[150:153], v[190:193], v[6:9]
	v_mfma_f32_16x16x32_bf16 v[2:5], v[158:161], v[190:193], v[2:5]
	s_setprio 0
	s_barrier
	s_branch .Lmid1440

.Lmid1440:
	ds_read_b128 v[130:133], v237
	ds_read_b128 v[134:137], v237 offset:1024
	ds_read_b128 v[138:141], v237 offset:2048
	ds_read_b128 v[142:145], v237 offset:3072
	ds_read_b128 v[146:149], v238
	ds_read_b128 v[150:153], v238 offset:1024
	ds_read_b128 v[154:157], v238 offset:2048
	ds_read_b128 v[158:161], v238 offset:3072
	ds_read_b128 v[162:165], v236 offset:32768
	ds_read_b128 v[166:169], v236 offset:33792
	ds_read_b128 v[170:173], v236 offset:34816
	ds_read_b128 v[174:177], v236 offset:35840
	ds_read_b128 v[178:181], v236 offset:36864
	ds_read_b128 v[182:185], v236 offset:37888
	ds_read_b128 v[186:189], v236 offset:38912
	ds_read_b128 v[190:193], v236 offset:39936
	s_add_u32 s58, s66, 0x40000
	s_addc_u32 s59, s67, 0
	s_mov_b32 s66, m0
	s_mov_b32 m0, s37
	s_nop 2
	global_load_lds_dwordx4 v228, s[58:59]
	s_mov_b32 m0, s66
	s_nop 0
	s_mov_b32 s66, m0
	s_mov_b32 m0, s52
	s_nop 2
	global_load_lds_dwordx4 v230, s[58:59]
	s_mov_b32 m0, s66
	s_waitcnt vmcnt(8)
	s_waitcnt lgkmcnt(0)
	s_barrier
	s_setprio 1
	s_waitcnt lgkmcnt(7)
	v_mfma_f32_16x16x32_bf16 v[126:129], v[130:133], v[162:165], v[126:129]
	v_mfma_f32_16x16x32_bf16 v[122:125], v[138:141], v[162:165], v[122:125]
	s_waitcnt lgkmcnt(5)
	v_mfma_f32_16x16x32_bf16 v[114:117], v[130:133], v[170:173], v[114:117]
	v_mfma_f32_16x16x32_bf16 v[106:109], v[138:141], v[170:173], v[106:109]
	s_waitcnt lgkmcnt(3)
	v_mfma_f32_16x16x32_bf16 v[94:97], v[130:133], v[178:181], v[94:97]
	v_mfma_f32_16x16x32_bf16 v[90:93], v[138:141], v[178:181], v[90:93]
	s_waitcnt lgkmcnt(1)
	v_mfma_f32_16x16x32_bf16 v[86:89], v[130:133], v[186:189], v[86:89]
	v_mfma_f32_16x16x32_bf16 v[78:81], v[138:141], v[186:189], v[78:81]
	v_mfma_f32_16x16x32_bf16 v[126:129], v[134:137], v[166:169], v[126:129]
	v_mfma_f32_16x16x32_bf16 v[122:125], v[142:145], v[166:169], v[122:125]
	v_mfma_f32_16x16x32_bf16 v[114:117], v[134:137], v[174:177], v[114:117]
	v_mfma_f32_16x16x32_bf16 v[106:109], v[142:145], v[174:177], v[106:109]
	v_mfma_f32_16x16x32_bf16 v[94:97], v[134:137], v[182:185], v[94:97]
	v_mfma_f32_16x16x32_bf16 v[90:93], v[142:145], v[182:185], v[90:93]
	s_waitcnt lgkmcnt(0)
	v_mfma_f32_16x16x32_bf16 v[86:89], v[134:137], v[190:193], v[86:89]
	v_mfma_f32_16x16x32_bf16 v[78:81], v[142:145], v[190:193], v[78:81]
	s_setprio 0
	s_setprio 1
	v_mfma_f32_16x16x32_bf16 v[118:121], v[146:149], v[162:165], v[118:121]
	v_mfma_f32_16x16x32_bf16 v[110:113], v[154:157], v[162:165], v[110:113]
	v_mfma_f32_16x16x32_bf16 v[102:105], v[146:149], v[170:173], v[102:105]
	v_mfma_f32_16x16x32_bf16 v[98:101], v[154:157], v[170:173], v[98:101]
	v_mfma_f32_16x16x32_bf16 v[82:85], v[146:149], v[178:181], v[82:85]
	v_mfma_f32_16x16x32_bf16 v[74:77], v[154:157], v[178:181], v[74:77]
	v_mfma_f32_16x16x32_bf16 v[70:73], v[146:149], v[186:189], v[70:73]
	v_mfma_f32_16x16x32_bf16 v[66:69], v[154:157], v[186:189], v[66:69]
	v_mfma_f32_16x16x32_bf16 v[118:121], v[150:153], v[166:169], v[118:121]
	v_mfma_f32_16x16x32_bf16 v[110:113], v[158:161], v[166:169], v[110:113]
	v_mfma_f32_16x16x32_bf16 v[102:105], v[150:153], v[174:177], v[102:105]
	v_mfma_f32_16x16x32_bf16 v[98:101], v[158:161], v[174:177], v[98:101]
	v_mfma_f32_16x16x32_bf16 v[82:85], v[150:153], v[182:185], v[82:85]
	v_mfma_f32_16x16x32_bf16 v[74:77], v[158:161], v[182:185], v[74:77]
	v_mfma_f32_16x16x32_bf16 v[70:73], v[150:153], v[190:193], v[70:73]
	v_mfma_f32_16x16x32_bf16 v[66:69], v[158:161], v[190:193], v[66:69]
	s_setprio 0
	s_barrier
	ds_read_b128 v[162:165], v236 offset:49152
	ds_read_b128 v[166:169], v236 offset:50176
	ds_read_b128 v[170:173], v236 offset:51200
	ds_read_b128 v[174:177], v236 offset:52224
	ds_read_b128 v[178:181], v236 offset:53248
	ds_read_b128 v[182:185], v236 offset:54272
	ds_read_b128 v[186:189], v236 offset:55296
	ds_read_b128 v[190:193], v236 offset:56320
	s_add_u32 s58, s64, 0x80
	s_addc_u32 s59, s65, 0
	s_mov_b32 s66, m0
	s_mov_b32 m0, s68
	s_nop 2
	global_load_lds_dwordx4 v229, s[58:59]
	s_mov_b32 m0, s66
	s_nop 0
	s_mov_b32 s66, m0
	s_mov_b32 m0, s69
	s_nop 2
	global_load_lds_dwordx4 v231, s[58:59]
	s_mov_b32 m0, s66
	s_add_u32 s58, s64, 0x40080
	s_addc_u32 s59, s65, 0
	s_mov_b32 s64, m0
	s_mov_b32 m0, s78
	s_nop 2
	global_load_lds_dwordx4 v229, s[58:59]
	s_mov_b32 m0, s64
	s_nop 0
	s_mov_b32 s64, m0
	s_mov_b32 m0, s79
	s_nop 2
	global_load_lds_dwordx4 v231, s[58:59]
	s_mov_b32 m0, s64
	s_mov_b32 s58, m0
	s_mov_b32 m0, s76
	s_nop 2
	global_load_lds_dwordx4 v228, s[62:63]
	s_mov_b32 m0, s58
	s_nop 0
	s_mov_b32 s58, m0
	s_mov_b32 m0, s77
	s_nop 2
	global_load_lds_dwordx4 v230, s[62:63]
	s_mov_b32 m0, s58
	s_waitcnt vmcnt(8)
	s_waitcnt lgkmcnt(0)
	s_barrier
	s_setprio 1
	s_waitcnt lgkmcnt(7)
	v_mfma_f32_16x16x32_bf16 v[62:65], v[130:133], v[162:165], v[62:65]
	v_mfma_f32_16x16x32_bf16 v[58:61], v[138:141], v[162:165], v[58:61]
	s_waitcnt lgkmcnt(5)
	v_mfma_f32_16x16x32_bf16 v[54:57], v[130:133], v[170:173], v[54:57]
	v_mfma_f32_16x16x32_bf16 v[46:49], v[138:141], v[170:173], v[46:49]
	s_waitcnt lgkmcnt(3)
	v_mfma_f32_16x16x32_bf16 v[38:41], v[130:133], v[178:181], v[38:41]
	v_mfma_f32_16x16x32_bf16 v[30:33], v[138:141], v[178:181], v[30:33]
	s_waitcnt lgkmcnt(1)
	v_mfma_f32_16x16x32_bf16 v[22:25], v[130:133], v[186:189], v[22:25]
	v_mfma_f32_16x16x32_bf16 v[14:17], v[138:141], v[186:189], v[14:17]
	v_mfma_f32_16x16x32_bf16 v[62:65], v[134:137], v[166:169], v[62:65]
	v_mfma_f32_16x16x32_bf16 v[58:61], v[142:145], v[166:169], v[58:61]
	v_mfma_f32_16x16x32_bf16 v[54:57], v[134:137], v[174:177], v[54:57]
	v_mfma_f32_16x16x32_bf16 v[46:49], v[142:145], v[174:177], v[46:49]
	v_mfma_f32_16x16x32_bf16 v[38:41], v[134:137], v[182:185], v[38:41]
	v_mfma_f32_16x16x32_bf16 v[30:33], v[142:145], v[182:185], v[30:33]
	s_waitcnt lgkmcnt(0)
	v_mfma_f32_16x16x32_bf16 v[22:25], v[134:137], v[190:193], v[22:25]
	v_mfma_f32_16x16x32_bf16 v[14:17], v[142:145], v[190:193], v[14:17]
	s_setprio 0
	s_setprio 1
	v_mfma_f32_16x16x32_bf16 v[50:53], v[146:149], v[162:165], v[50:53]
	v_mfma_f32_16x16x32_bf16 v[42:45], v[154:157], v[162:165], v[42:45]
	v_mfma_f32_16x16x32_bf16 v[34:37], v[146:149], v[170:173], v[34:37]
	v_mfma_f32_16x16x32_bf16 v[26:29], v[154:157], v[170:173], v[26:29]
	v_mfma_f32_16x16x32_bf16 v[18:21], v[146:149], v[178:181], v[18:21]
	v_mfma_f32_16x16x32_bf16 v[10:13], v[154:157], v[178:181], v[10:13]
	v_mfma_f32_16x16x32_bf16 v[6:9], v[146:149], v[186:189], v[6:9]
	v_mfma_f32_16x16x32_bf16 v[2:5], v[154:157], v[186:189], v[2:5]
	v_mfma_f32_16x16x32_bf16 v[50:53], v[150:153], v[166:169], v[50:53]
	v_mfma_f32_16x16x32_bf16 v[42:45], v[158:161], v[166:169], v[42:45]
	v_mfma_f32_16x16x32_bf16 v[34:37], v[150:153], v[174:177], v[34:37]
	v_mfma_f32_16x16x32_bf16 v[26:29], v[158:161], v[174:177], v[26:29]
	v_mfma_f32_16x16x32_bf16 v[18:21], v[150:153], v[182:185], v[18:21]
	v_mfma_f32_16x16x32_bf16 v[10:13], v[158:161], v[182:185], v[10:13]
	v_mfma_f32_16x16x32_bf16 v[6:9], v[150:153], v[190:193], v[6:9]
	v_mfma_f32_16x16x32_bf16 v[2:5], v[158:161], v[190:193], v[2:5]
	s_setprio 0
	s_barrier
	s_add_i32 s87, s87, 2
	s_add_u32 s85, s85, 0x100
	s_addc_u32 s86, s86, 0
	s_cmp_gt_u32 s87, 13
	s_mov_b64 s[58:59], s[60:61]
	s_cbranch_scc0 .LBB0_1440
	s_and_b64 vcc, exec, s[16:17]
	s_cbranch_vccz .LBB0_1443
	s_barrier

.LBB0_1889:
	s_add_u32 s8, s74, 0x20000
	v_and_b32_e32 v166, 15, v0
	v_and_b32_e32 v2, 48, v0
	v_lshlrev_b32_e32 v4, 2, v0
	v_writelane_b32 v253, s8, 8
	s_addc_u32 s8, s75, 0
	s_lshl_b32 s82, s5, 6
	v_lshl_or_b32 v3, v166, 6, v2
	s_lshl_b32 s5, s5, 13
	v_and_b32_e32 v4, 32, v4
	v_bitop3_b32 v3, v3, s5, v4 bitop3:0xde
	s_lshl_b32 s5, s66, 5
	s_and_b32 s83, s5, 0x60
	v_lshlrev_b32_e32 v5, 6, v0
	s_movk_i32 s5, 0x3c0
	v_and_or_b32 v2, v5, s5, v2
	s_lshl_b32 s5, s83, 7
	v_writelane_b32 v253, s8, 31
	s_add_u32 s8, s40, 0x80
	v_bitop3_b32 v2, s5, v2, v4 bitop3:0xf6
	s_waitcnt vmcnt(2)
	s_barrier
	s_addc_u32 s9, s41, 0
	s_add_i32 s84, s15, 0x18000
	s_mov_b32 s5, m0
	s_mov_b32 m0, s84
	s_nop 2
	global_load_lds_dwordx4 v1, s[8:9]
	s_mov_b32 m0, s5
	s_add_i32 s85, s15, 0x1a000
	s_mov_b32 s5, m0
	s_mov_b32 m0, s85
	s_nop 2
	global_load_lds_dwordx4 v163, s[8:9]
	s_mov_b32 m0, s5
	s_add_u32 s8, s74, 0x1d800080
	s_addc_u32 s9, s75, 0
	s_add_i32 s86, s15, 0x8000
	s_mov_b32 s5, m0
	s_mov_b32 m0, s86
	s_nop 2
	global_load_lds_dwordx4 v168, s[8:9]
	s_mov_b32 m0, s5
	s_add_i32 s87, s15, 0xa000
	s_mov_b32 s5, m0
	s_mov_b32 m0, s87
	s_nop 2
	global_load_lds_dwordx4 v172, s[8:9]
	s_mov_b32 m0, s5
	s_add_u32 s8, s40, 0x20080
	s_addc_u32 s9, s41, 0
	s_add_i32 s91, s15, 0x1c000
	s_mov_b32 s5, m0
	s_mov_b32 m0, s91
	s_nop 2
	global_load_lds_dwordx4 v1, s[8:9]
	s_mov_b32 m0, s5
	s_add_i32 s92, s15, 0x1e000
	s_add_i32 s93, s15, 0xc000
	s_mov_b32 s5, m0
	s_mov_b32 m0, s92
	s_nop 2
	global_load_lds_dwordx4 v163, s[8:9]
	s_mov_b32 m0, s5
	s_cmpk_lt_u32 s4, 0x100
	s_waitcnt vmcnt(6)
	s_cselect_b64 s[16:17], -1, 0
	s_add_i32 s94, s15, 0xe000
	s_lshr_b32 s2, s2, 5
	s_and_b64 s[6:7], s[6:7], exec
	v_mov_b32_e32 v171, 0
	v_lshrrev_b32_e32 v167, 4, v218
	s_mov_b32 s88, 0
	v_lshlrev_b32_e32 v170, 4, v218
	v_cmp_eq_u32_e64 s[4:5], 0, v218
	s_cselect_b32 s95, s2, 0
	v_writelane_b32 v253, s20, 45
	s_bfe_u32 s96, s20, 0x50003
	s_add_i32 s97, 0, 0x201c0
	s_xor_b64 s[18:19], s[18:19], -1
	v_add_u32_e32 v173, 0, v2
	v_add_u32_e32 v174, 0, v3
	s_mov_b32 s37, 0xc0e00000
	s_mov_b32 s20, 0xc01d265f
	v_mov_b32_e32 v176, 0x40e00000
	v_mov_b32_e32 v177, v175
	v_mov_b32_e32 v178, v169
	s_mov_b32 s36, s30
	v_mov_b32_e32 v34, 0
	v_mov_b32_e32 v35, v171
	v_mov_b32_e32 v36, v171
	v_mov_b32_e32 v37, v171
	v_mov_b32_e32 v38, 0
	v_mov_b32_e32 v39, v171
	v_mov_b32_e32 v40, v171
	v_mov_b32_e32 v41, v171
	v_mov_b32_e32 v42, 0
	v_mov_b32_e32 v43, v171
	v_mov_b32_e32 v44, v171
	v_mov_b32_e32 v45, v171
	v_mov_b32_e32 v46, 0
	v_mov_b32_e32 v47, v171
	v_mov_b32_e32 v48, v171
	v_mov_b32_e32 v49, v171
	v_mov_b32_e32 v50, 0
	v_mov_b32_e32 v51, v171
	v_mov_b32_e32 v52, v171
	v_mov_b32_e32 v53, v171
	v_mov_b32_e32 v54, 0
	v_mov_b32_e32 v55, v171
	v_mov_b32_e32 v56, v171
	v_mov_b32_e32 v57, v171
	v_mov_b32_e32 v58, 0
	v_mov_b32_e32 v59, v171
	v_mov_b32_e32 v60, v171
	v_mov_b32_e32 v61, v171
	v_mov_b32_e32 v62, 0
	v_mov_b32_e32 v63, v171
	v_mov_b32_e32 v64, v171
	v_mov_b32_e32 v65, v171
	v_mov_b32_e32 v66, 0
	v_mov_b32_e32 v67, v171
	v_mov_b32_e32 v68, v171
	v_mov_b32_e32 v69, v171
	v_mov_b32_e32 v70, 0
	v_mov_b32_e32 v71, v171
	v_mov_b32_e32 v72, v171
	v_mov_b32_e32 v73, v171
	v_mov_b32_e32 v74, 0
	v_mov_b32_e32 v75, v171
	v_mov_b32_e32 v76, v171
	v_mov_b32_e32 v77, v171
	v_mov_b32_e32 v78, 0
	v_mov_b32_e32 v79, v171
	v_mov_b32_e32 v80, v171
	v_mov_b32_e32 v81, v171
	v_mov_b32_e32 v82, 0
	v_mov_b32_e32 v83, v171
	v_mov_b32_e32 v84, v171
	v_mov_b32_e32 v85, v171
	v_mov_b32_e32 v86, 0
	v_mov_b32_e32 v87, v171
	v_mov_b32_e32 v88, v171
	v_mov_b32_e32 v89, v171
	v_mov_b32_e32 v90, 0
	v_mov_b32_e32 v91, v171
	v_mov_b32_e32 v92, v171
	v_mov_b32_e32 v93, v171
	v_mov_b32_e32 v94, 0
	v_mov_b32_e32 v95, v171
	v_mov_b32_e32 v96, v171
	v_mov_b32_e32 v97, v171
	v_mov_b32_e32 v98, 0
	v_mov_b32_e32 v99, v171
	v_mov_b32_e32 v100, v171
	v_mov_b32_e32 v101, v171
	v_mov_b32_e32 v102, 0
	v_mov_b32_e32 v103, v171
	v_mov_b32_e32 v104, v171
	v_mov_b32_e32 v105, v171
	v_mov_b32_e32 v106, 0
	v_mov_b32_e32 v107, v171
	v_mov_b32_e32 v108, v171
	v_mov_b32_e32 v109, v171
	v_mov_b32_e32 v110, 0
	v_mov_b32_e32 v111, v171
	v_mov_b32_e32 v112, v171
	v_mov_b32_e32 v113, v171
	v_mov_b32_e32 v114, 0
	v_mov_b32_e32 v115, v171
	v_mov_b32_e32 v116, v171
	v_mov_b32_e32 v117, v171
	v_mov_b32_e32 v118, 0
	v_mov_b32_e32 v119, v171
	v_mov_b32_e32 v120, v171
	v_mov_b32_e32 v121, v171
	v_mov_b32_e32 v122, 0
	v_mov_b32_e32 v123, v171
	v_mov_b32_e32 v124, v171
	v_mov_b32_e32 v125, v171
	v_mov_b32_e32 v126, 0
	v_mov_b32_e32 v127, v171
	v_mov_b32_e32 v128, v171
	v_mov_b32_e32 v129, v171
	v_mov_b32_e32 v130, 0
	v_mov_b32_e32 v131, v171
	v_mov_b32_e32 v132, v171
	v_mov_b32_e32 v133, v171
	v_mov_b32_e32 v134, 0
	v_mov_b32_e32 v135, v171
	v_mov_b32_e32 v136, v171
	v_mov_b32_e32 v137, v171
	v_mov_b32_e32 v138, 0
	v_mov_b32_e32 v139, v171
	v_mov_b32_e32 v140, v171
	v_mov_b32_e32 v141, v171
	v_mov_b32_e32 v142, 0
	v_mov_b32_e32 v143, v171
	v_mov_b32_e32 v144, v171
	v_mov_b32_e32 v145, v171
	v_mov_b32_e32 v146, 0
	v_mov_b32_e32 v147, v171
	v_mov_b32_e32 v148, v171
	v_mov_b32_e32 v149, v171
	v_mov_b32_e32 v150, 0
	v_mov_b32_e32 v151, v171
	v_mov_b32_e32 v152, v171
	v_mov_b32_e32 v153, v171
	v_mov_b32_e32 v154, 0
	v_mov_b32_e32 v155, v171
	v_mov_b32_e32 v156, v171
	v_mov_b32_e32 v157, v171
	v_mov_b32_e32 v158, 0
	v_mov_b32_e32 v159, v171
	v_mov_b32_e32 v160, v171
	v_mov_b32_e32 v161, v171
	s_barrier
	v_lshrrev_b32_e32 v212, 6, v0
	v_and_b32_e32 v213, 63, v0
	v_lshlrev_b32_e32 v213, 4, v213
	v_lshrrev_b32_e32 v214, 4, v213
	v_and_b32_e32 v214, 32, v214
	v_xor_b32_e32 v213, v214, v213
	v_lshrrev_b32_e32 v214, 6, v213
	v_lshrrev_b32_e32 v215, 1, v212
	v_lshl_add_u32 v214, v215, 4, v214
	v_and_b32_e32 v212, 1, v212
	v_and_b32_e32 v213, 62, v213
	v_lshl_add_u32 v213, v212, 6, v213
	v_lshlrev_b32_e32 v212, 2, v214

.LBB0_1900:
	s_andn2_b64 vcc, exec, s[42:43]
	s_cbranch_vccnz .LBB0_1895
	v_add_u32_e32 v2, s25, v212
	ds_read2st64_b32 v[4:5], v2 offset1:2
	ds_read2st64_b32 v[6:7], v2 offset0:1 offset1:3
	s_waitcnt lgkmcnt(0)
	v_min_u32_e32 v4, 0x3fff, v4
	v_min_u32_e32 v5, 0x3fff, v5
	v_min_u32_e32 v6, 0x3fff, v6
	v_min_u32_e32 v7, 0x3fff, v7
	v_lshl_add_u32 v168, v4, 10, v213
	v_lshl_add_u32 v169, v5, 10, v213
	v_lshl_add_u32 v172, v6, 10, v213
	v_lshl_add_u32 v175, v7, 10, v213
	s_branch .LBB0_1895
